# baseline (speedup 1.0000x reference)
_Z16closed_form_mainPKfS0_PKiPf:
	s_load_dwordx8 s[16:23], s[0:1], 0x0
	s_lshr_b32 s6, s2, 3
	v_readfirstlane_b32 s0, v0
	s_mul_hi_u32 s7, s6, 0x24924925
	s_lshr_b32 s4, s0, 6
	s_and_b32 s0, s2, 7
	s_mul_i32 s1, s7, 7
	s_bfe_u32 s5, s2, 0x10003
	s_sub_i32 s1, s6, s1
	s_mul_i32 s36, s0, 7
	s_xor_b32 s3, s4, s5
	s_add_i32 s36, s36, s1
	s_waitcnt lgkmcnt(0)
	s_mov_b64 s[28:29], s[22:23]
	v_and_b32_e32 v19, 63, v0
	s_cmp_lt_u32 s36, 52
	s_mov_b64 s[0:1], -1
	s_cbranch_scc0 .LBB0_32
	s_mul_hi_u32 s0, s6, 0x20820821
	s_lshr_b32 s38, s0, 3
	s_mul_hi_u32 s0, s7, 0x1c71c71d
	s_mul_i32 s0, s0, 9
	s_sub_i32 s0, s7, s0
	v_add_u32_e32 v2, -3, v19
	v_mad_u64_u32 v[0:1], s[0:1], s0, 57, v[2:3]
	s_mov_b64 s[24:25], s[18:19]
	v_mov_b32_e32 v1, 0x200
	v_med3_i32 v1, v0, 0, v1
	s_mul_i32 s34, s36, 10
	s_and_b32 s17, s17, 0xffff
	s_and_b32 s25, s25, 0xffff
	v_cmp_gt_u32_e64 s[0:1], 57, v2
	s_mov_b32 s19, 0x20000
	s_mov_b32 s18, 0xe0e038
	s_mov_b32 s26, 0x606018
	s_mul_i32 s35, s38, 0x70701c
	s_mul_i32 s33, s38, 0x30300c
	v_lshlrev_b32_e32 v28, 2, v1
	v_mul_u32_u24_e32 v27, 12, v1
	v_lshlrev_b32_e32 v23, 4, v19
	s_cmp_lg_u32 s4, s5
	v_sub_u32_e64 v29, s34, 2 clamp
	s_cbranch_scc0 .LBB0_15
	s_setprio 2
	s_mov_b32 s27, s19
	s_and_b32 s21, s21, 0xffff
	s_mov_b32 s22, 0x202008
	s_mov_b32 s23, s19
	s_mul_i32 s38, s38, 0x101004
	s_movk_i32 s37, 0x80
	v_add_u32_e32 v18, -1, v0
	s_movk_i32 s4, 0x201
	s_movk_i32 s5, 0x1ff
	v_cmp_gt_u32_e64 s[40:41], s4, v0
	v_cmp_gt_u32_e64 s[42:43], s5, v18
	v_mov_b32_e32 v18, 0x42c80000
	v_mov_b32_e32 v22, 0x3de38e39
	v_mov_b32_e32 v26, 0x3a3d6628
	v_mov_b32_e32 v1, 0
	s_add_i32 s4, s34, -3
	s_max_i32 s4, s4, 0
	s_mul_i32 s4, s4, 0x804
	s_add_i32 s4, s4, s38
	buffer_load_dword v29, v28, s[20:23], s4 offen nt
	s_add_i32 s4, s34, -2
	s_max_i32 s4, s4, 0
	s_mul_i32 s4, s4, 0x804
	s_add_i32 s4, s4, s38
	buffer_load_dword v2, v28, s[20:23], s4 offen nt
	s_add_i32 s5, s34, -2
	s_max_i32 s5, s5, 0
	s_mul_i32 s6, s5, 0x804
	s_add_i32 s6, s6, s35
	s_add_i32 s7, s6, 0x505014
	s_add_i32 s8, s6, 0x606018
	s_mul_i32 s9, s5, 0x180c
	s_add_i32 s9, s9, s33
	s_add_i32 s4, s34, -1
	s_max_i32 s4, s4, 0
	s_mul_i32 s4, s4, 0x804
	s_add_i32 s4, s4, s38
	buffer_load_dword v3, v28, s[20:23], s4 offen nt
	buffer_load_dwordx3 v[8:10], v27, s[24:27], s9 offen nt
	buffer_load_dword v4, v28, s[16:19], s7 offen nt
	buffer_load_dword v5, v28, s[16:19], s8 offen nt
	s_add_i32 s5, s34, -1
	s_max_i32 s5, s5, 0
	s_mul_i32 s6, s5, 0x804
	s_add_i32 s6, s6, s35
	s_add_i32 s7, s6, 0x505014
	s_add_i32 s8, s6, 0x606018
	s_mul_i32 s9, s5, 0x180c
	s_add_i32 s9, s9, s33
	s_add_i32 s4, s34, 0
	s_min_i32 s4, s4, 0x200
	s_mul_i32 s4, s4, 0x804
	s_add_i32 s4, s4, s38
	buffer_load_dword v16, v28, s[20:23], s4 offen nt
	buffer_load_dwordx3 v[12:14], v27, s[24:27], s9 offen nt
	buffer_load_dword v6, v28, s[16:19], s7 offen nt
	buffer_load_dword v7, v28, s[16:19], s8 offen nt
	s_waitcnt vmcnt(8)
	s_add_i32 s4, s34, -3
	s_cmpk_lt_u32 s4, 0x201
	s_cselect_b64 s[12:13], s[40:41], 0
	v_cmp_eq_u32_e64 s[14:15], s37, v29
	s_and_b64 s[14:15], s[14:15], s[12:13]
	v_cndmask_b32_e64 v17, 0, 1, s[14:15]
	s_add_i32 s4, s34, -2
	s_cmpk_lt_u32 s4, 0x201
	s_cselect_b64 s[12:13], s[40:41], 0
	v_cmp_eq_u32_e64 s[14:15], s37, v2
	s_and_b64 s[14:15], s[14:15], s[12:13]
	v_cndmask_b32_e64 v20, 0, 1, s[14:15]
	s_nop 0
	v_or_b32_dpp v21, v17, v17 wave_shr:1 row_mask:0xf bank_mask:0xf bound_ctrl:1
	v_or_b32_dpp v24, v20, v20 wave_shr:1 row_mask:0xf bank_mask:0xf bound_ctrl:1
	s_nop 1
	v_or_b32_dpp v21, v17, v21 wave_shl:1 row_mask:0xf bank_mask:0xf bound_ctrl:1
	v_or_b32_dpp v24, v20, v24 wave_shl:1 row_mask:0xf bank_mask:0xf bound_ctrl:1
	s_nop 1
	v_or_b32_dpp v25, v21, v21 wave_shr:1 row_mask:0xf bank_mask:0xf bound_ctrl:1
	v_or_b32_dpp v30, v24, v24 wave_shr:1 row_mask:0xf bank_mask:0xf bound_ctrl:1
	s_nop 1
	v_or_b32_dpp v25, v21, v25 wave_shl:1 row_mask:0xf bank_mask:0xf bound_ctrl:1
	v_or_b32_dpp v30, v24, v30 wave_shl:1 row_mask:0xf bank_mask:0xf bound_ctrl:1
	v_mov_b32_e32 v17, 0
	v_mov_b32_e32 v24, 0
	s_add_i32 s5, s34, 0
	s_min_i32 s5, s5, 0x200
	s_mul_i32 s6, s5, 0x804
	s_add_i32 s6, s6, s35
	s_add_i32 s7, s6, 0x505014
	s_add_i32 s8, s6, 0x606018
	s_mul_i32 s9, s5, 0x180c
	s_add_i32 s9, s9, s33
	s_add_i32 s4, s34, 1
	s_min_i32 s4, s4, 0x200
	s_mul_i32 s4, s4, 0x804
	s_add_i32 s4, s4, s38
	buffer_load_dword v31, v28, s[20:23], s4 offen nt
	buffer_load_dwordx3 v[32:34], v27, s[24:27], s9 offen nt
	buffer_load_dword v20, v28, s[16:19], s7 offen nt
	buffer_load_dword v21, v28, s[16:19], s8 offen nt
	s_waitcnt vmcnt(8)
	v_mov_b32_dpp v36, v8 wave_shr:1 row_mask:0xf bank_mask:0xf bound_ctrl:1
	v_mov_b32_dpp v37, v9 wave_shr:1 row_mask:0xf bank_mask:0xf bound_ctrl:1
	v_mov_b32_dpp v38, v10 wave_shr:1 row_mask:0xf bank_mask:0xf bound_ctrl:1
	v_mov_b32_dpp v40, v8 wave_shl:1 row_mask:0xf bank_mask:0xf bound_ctrl:1
	v_mov_b32_dpp v41, v9 wave_shl:1 row_mask:0xf bank_mask:0xf bound_ctrl:1
	v_mov_b32_dpp v42, v10 wave_shl:1 row_mask:0xf bank_mask:0xf bound_ctrl:1
	s_add_i32 s4, s34, -1
	s_cmpk_lt_u32 s4, 0x201
	s_cselect_b64 s[12:13], s[40:41], 0
	v_cmp_eq_u32_e64 s[14:15], s37, v3
	s_and_b64 s[14:15], s[14:15], s[12:13]
	v_cndmask_b32_e64 v44, 0, 1, s[14:15]
	v_mul_f32_e64 v46, v8, v8
	v_mul_f32_e64 v47, v8, v9
	v_or_b32_dpp v45, v44, v44 wave_shr:1 row_mask:0xf bank_mask:0xf bound_ctrl:1
	v_mul_f32_e64 v48, v8, v10
	v_or_b32_dpp v45, v44, v45 wave_shl:1 row_mask:0xf bank_mask:0xf bound_ctrl:1
	v_mul_f32_e64 v49, v9, v9
	v_mul_f32_e64 v50, v9, v10
	v_or_b32_dpp v52, v45, v45 wave_shr:1 row_mask:0xf bank_mask:0xf bound_ctrl:1
	v_mul_f32_e64 v51, v10, v10
	s_nop 0
	v_or_b32_dpp v52, v45, v52 wave_shl:1 row_mask:0xf bank_mask:0xf bound_ctrl:1
	v_or3_b32 v53, v52, v30, v25
	v_or3_b32 v53, v53, v17, v24
	s_add_i32 s4, s34, -4
	s_cmpk_lt_u32 s4, 0x1ff
	s_cselect_b64 s[12:13], s[42:43], 0
	v_cmp_ne_u32_e64 s[30:31], 0, v53
	s_and_b64 s[30:31], s[30:31], s[12:13]
	v_cndmask_b32_e64 v53, 0, 1.0, s[30:31]
	v_add_f32_e64 v44, v8, v36
	v_add_f32_e64 v45, v9, v37
	v_add_f32_e64 v54, v10, v38
	v_fma_f32 v46, v36, v36, v46
	v_fma_f32 v47, v36, v37, v47
	v_fma_f32 v48, v36, v38, v48
	v_fma_f32 v49, v37, v37, v49
	v_fma_f32 v50, v37, v38, v50
	v_fma_f32 v51, v38, v38, v51
	v_add_f32_dpp v61, v53, v53 wave_shr:1 row_mask:0xf bank_mask:0xf bound_ctrl:1
	v_add_f32_e64 v44, v44, v40
	v_add_f32_e64 v45, v45, v41
	v_add_f32_e64 v54, v54, v42
	v_fma_f32 v55, v40, v40, v46
	v_fma_f32 v56, v40, v41, v47
	v_fma_f32 v57, v40, v42, v48
	v_fma_f32 v58, v41, v41, v49
	v_fma_f32 v59, v41, v42, v50
	v_fma_f32 v60, v42, v42, v51
	v_add_f32_dpp v61, v53, v61 wave_shl:1 row_mask:0xf bank_mask:0xf bound_ctrl:1
	v_mov_b32_dpp v46, v4 wave_shr:1 row_mask:0xf bank_mask:0xf bound_ctrl:1
	v_mov_b32_dpp v47, v5 wave_shr:1 row_mask:0xf bank_mask:0xf bound_ctrl:1
	v_mov_b32_dpp v48, v4 wave_shl:1 row_mask:0xf bank_mask:0xf bound_ctrl:1
	v_mov_b32_dpp v49, v5 wave_shl:1 row_mask:0xf bank_mask:0xf bound_ctrl:1
	v_pk_mul_f32 v[50:51], v[4:5], v[8:9] op_sel_hi:[1,0]
	v_pk_mul_f32 v[62:63], v[4:5], v[8:9] op_sel:[0,1]
	v_pk_mul_f32 v[64:65], v[4:5], v[10:11] op_sel_hi:[1,0]
	v_pk_add_f32 v[66:67], v[4:5], v[46:47]
	v_pk_fma_f32 v[50:51], v[46:47], v[36:37], v[50:51] op_sel_hi:[1,0,1]
	v_pk_fma_f32 v[62:63], v[46:47], v[36:37], v[62:63] op_sel:[0,1,0]
	v_pk_fma_f32 v[64:65], v[46:47], v[38:39], v[64:65] op_sel_hi:[1,0,1]
	v_pk_add_f32 v[66:67], v[66:67], v[48:49]
	v_pk_fma_f32 v[50:51], v[48:49], v[40:41], v[50:51] op_sel_hi:[1,0,1]
	v_pk_fma_f32 v[62:63], v[48:49], v[40:41], v[62:63] op_sel:[0,1,0]
	v_pk_fma_f32 v[64:65], v[48:49], v[42:43], v[64:65] op_sel_hi:[1,0,1]
	s_barrier
	s_add_i32 s5, s34, 1
	s_min_i32 s5, s5, 0x200
	s_mul_i32 s6, s5, 0x804
	s_add_i32 s6, s6, s35
	s_add_i32 s7, s6, 0x505014
	s_add_i32 s8, s6, 0x606018
	s_mul_i32 s9, s5, 0x180c
	s_add_i32 s9, s9, s33
	s_add_i32 s4, s34, 2
	s_min_i32 s4, s4, 0x200
	s_mul_i32 s4, s4, 0x804
	s_add_i32 s4, s4, s38
	buffer_load_dword v24, v28, s[20:23], s4 offen nt
	buffer_load_dwordx3 v[68:70], v27, s[24:27], s9 offen nt
	buffer_load_dword v46, v28, s[16:19], s7 offen nt
	buffer_load_dword v47, v28, s[16:19], s8 offen nt
	s_waitcnt vmcnt(8)
	v_mov_b32_dpp v72, v12 wave_shr:1 row_mask:0xf bank_mask:0xf bound_ctrl:1
	v_mov_b32_dpp v73, v13 wave_shr:1 row_mask:0xf bank_mask:0xf bound_ctrl:1
	v_mov_b32_dpp v74, v14 wave_shr:1 row_mask:0xf bank_mask:0xf bound_ctrl:1
	v_mov_b32_dpp v76, v12 wave_shl:1 row_mask:0xf bank_mask:0xf bound_ctrl:1
	v_mov_b32_dpp v77, v13 wave_shl:1 row_mask:0xf bank_mask:0xf bound_ctrl:1
	v_mov_b32_dpp v78, v14 wave_shl:1 row_mask:0xf bank_mask:0xf bound_ctrl:1
	s_add_i32 s4, s34, 0
	s_cmpk_lt_u32 s4, 0x201
	s_cselect_b64 s[12:13], s[40:41], 0
	v_cmp_eq_u32_e64 s[14:15], s37, v16
	s_and_b64 s[14:15], s[14:15], s[12:13]
	v_cndmask_b32_e64 v53, 0, 1, s[14:15]
	v_mul_f32_e64 v48, v12, v12
	v_mul_f32_e64 v49, v12, v13
	v_or_b32_dpp v84, v53, v53 wave_shr:1 row_mask:0xf bank_mask:0xf bound_ctrl:1
	v_mul_f32_e64 v80, v12, v14
	v_or_b32_dpp v84, v53, v84 wave_shl:1 row_mask:0xf bank_mask:0xf bound_ctrl:1
	v_mul_f32_e64 v81, v13, v13
	v_mul_f32_e64 v82, v13, v14
	v_or_b32_dpp v85, v84, v84 wave_shr:1 row_mask:0xf bank_mask:0xf bound_ctrl:1
	v_mul_f32_e64 v83, v14, v14
	s_nop 0
	v_or_b32_dpp v85, v84, v85 wave_shl:1 row_mask:0xf bank_mask:0xf bound_ctrl:1
	v_or3_b32 v53, v85, v52, v30
	v_or3_b32 v53, v53, v25, v17
	s_add_i32 s4, s34, -3
	s_cmpk_lt_u32 s4, 0x1ff
	s_cselect_b64 s[12:13], s[42:43], 0
	v_cmp_ne_u32_e64 s[30:31], 0, v53
	s_and_b64 s[30:31], s[30:31], s[12:13]
	v_cndmask_b32_e64 v53, 0, 1.0, s[30:31]
	v_add_f32_e64 v86, v12, v72
	v_add_f32_e64 v87, v13, v73
	v_add_f32_e64 v88, v14, v74
	v_fma_f32 v48, v72, v72, v48
	v_fma_f32 v49, v72, v73, v49
	v_fma_f32 v80, v72, v74, v80
	v_fma_f32 v81, v73, v73, v81
	v_fma_f32 v82, v73, v74, v82
	v_fma_f32 v83, v74, v74, v83
	v_add_f32_dpp v95, v53, v53 wave_shr:1 row_mask:0xf bank_mask:0xf bound_ctrl:1
	v_add_f32_e64 v86, v86, v76
	v_add_f32_e64 v87, v87, v77
	v_add_f32_e64 v88, v88, v78
	v_fma_f32 v89, v76, v76, v48
	v_fma_f32 v90, v76, v77, v49
	v_fma_f32 v91, v76, v78, v80
	v_fma_f32 v92, v77, v77, v81
	v_fma_f32 v93, v77, v78, v82
	v_fma_f32 v94, v78, v78, v83
	v_add_f32_dpp v95, v53, v95 wave_shl:1 row_mask:0xf bank_mask:0xf bound_ctrl:1
	v_mov_b32_dpp v48, v6 wave_shr:1 row_mask:0xf bank_mask:0xf bound_ctrl:1
	v_mov_b32_dpp v49, v7 wave_shr:1 row_mask:0xf bank_mask:0xf bound_ctrl:1
	v_mov_b32_dpp v80, v6 wave_shl:1 row_mask:0xf bank_mask:0xf bound_ctrl:1
	v_mov_b32_dpp v81, v7 wave_shl:1 row_mask:0xf bank_mask:0xf bound_ctrl:1
	v_pk_mul_f32 v[82:83], v[6:7], v[12:13] op_sel_hi:[1,0]
	v_pk_mul_f32 v[96:97], v[6:7], v[12:13] op_sel:[0,1]
	v_pk_mul_f32 v[98:99], v[6:7], v[14:15] op_sel_hi:[1,0]
	v_pk_add_f32 v[100:101], v[6:7], v[48:49]
	v_pk_fma_f32 v[82:83], v[48:49], v[72:73], v[82:83] op_sel_hi:[1,0,1]
	v_pk_fma_f32 v[96:97], v[48:49], v[72:73], v[96:97] op_sel:[0,1,0]
	v_pk_fma_f32 v[98:99], v[48:49], v[74:75], v[98:99] op_sel_hi:[1,0,1]
	v_pk_add_f32 v[100:101], v[100:101], v[80:81]
	v_pk_fma_f32 v[82:83], v[80:81], v[76:77], v[82:83] op_sel_hi:[1,0,1]
	v_pk_fma_f32 v[96:97], v[80:81], v[76:77], v[96:97] op_sel:[0,1,0]
	v_pk_fma_f32 v[98:99], v[80:81], v[78:79], v[98:99] op_sel_hi:[1,0,1]
	s_barrier
	s_add_i32 s5, s34, 2
	s_min_i32 s5, s5, 0x200
	s_mul_i32 s6, s5, 0x804
	s_add_i32 s6, s6, s35
	s_add_i32 s7, s6, 0x505014
	s_add_i32 s8, s6, 0x606018
	s_mul_i32 s9, s5, 0x180c
	s_add_i32 s9, s9, s33
	s_add_i32 s4, s34, 3
	s_min_i32 s4, s4, 0x200
	s_mul_i32 s4, s4, 0x804
	s_add_i32 s4, s4, s38
	buffer_load_dword v17, v28, s[20:23], s4 offen nt
	buffer_load_dwordx3 v[104:106], v27, s[24:27], s9 offen nt
	buffer_load_dword v48, v28, s[16:19], s7 offen nt
	buffer_load_dword v49, v28, s[16:19], s8 offen nt
	s_waitcnt vmcnt(8)
	v_mov_b32_dpp v108, v32 wave_shr:1 row_mask:0xf bank_mask:0xf bound_ctrl:1
	v_mov_b32_dpp v109, v33 wave_shr:1 row_mask:0xf bank_mask:0xf bound_ctrl:1
	v_mov_b32_dpp v110, v34 wave_shr:1 row_mask:0xf bank_mask:0xf bound_ctrl:1
	v_mov_b32_dpp v112, v32 wave_shl:1 row_mask:0xf bank_mask:0xf bound_ctrl:1
	v_mov_b32_dpp v113, v33 wave_shl:1 row_mask:0xf bank_mask:0xf bound_ctrl:1
	v_mov_b32_dpp v114, v34 wave_shl:1 row_mask:0xf bank_mask:0xf bound_ctrl:1
	s_add_i32 s4, s34, 1
	s_cmpk_lt_u32 s4, 0x201
	s_cselect_b64 s[12:13], s[40:41], 0
	v_cmp_eq_u32_e64 s[14:15], s37, v31
	s_and_b64 s[14:15], s[14:15], s[12:13]
	v_cndmask_b32_e64 v29, 0, 1, s[14:15]
	v_mul_f32_e64 v80, v32, v32
	v_mul_f32_e64 v81, v32, v33
	v_or_b32_dpp v53, v29, v29 wave_shr:1 row_mask:0xf bank_mask:0xf bound_ctrl:1
	v_mul_f32_e64 v102, v32, v34
	v_or_b32_dpp v53, v29, v53 wave_shl:1 row_mask:0xf bank_mask:0xf bound_ctrl:1
	v_mul_f32_e64 v103, v33, v33
	v_mul_f32_e64 v116, v33, v34
	v_or_b32_dpp v84, v53, v53 wave_shr:1 row_mask:0xf bank_mask:0xf bound_ctrl:1
	v_mul_f32_e64 v117, v34, v34
	s_nop 0
	v_or_b32_dpp v84, v53, v84 wave_shl:1 row_mask:0xf bank_mask:0xf bound_ctrl:1
	v_or3_b32 v29, v84, v85, v52
	v_or3_b32 v29, v29, v30, v25
	s_add_i32 s4, s34, -2
	s_cmpk_lt_u32 s4, 0x1ff
	s_cselect_b64 s[12:13], s[42:43], 0
	v_cmp_ne_u32_e64 s[30:31], 0, v29
	s_and_b64 s[30:31], s[30:31], s[12:13]
	v_cndmask_b32_e64 v29, 0, 1.0, s[30:31]
	v_add_f32_e64 v118, v32, v108
	v_add_f32_e64 v119, v33, v109
	v_add_f32_e64 v120, v34, v110
	v_fma_f32 v80, v108, v108, v80
	v_fma_f32 v81, v108, v109, v81
	v_fma_f32 v102, v108, v110, v102
	v_fma_f32 v103, v109, v109, v103
	v_fma_f32 v116, v109, v110, v116
	v_fma_f32 v117, v110, v110, v117
	v_add_f32_dpp v127, v29, v29 wave_shr:1 row_mask:0xf bank_mask:0xf bound_ctrl:1
	v_add_f32_e64 v118, v118, v112
	v_add_f32_e64 v119, v119, v113
	v_add_f32_e64 v120, v120, v114
	v_fma_f32 v121, v112, v112, v80
	v_fma_f32 v122, v112, v113, v81
	v_fma_f32 v123, v112, v114, v102
	v_fma_f32 v124, v113, v113, v103
	v_fma_f32 v125, v113, v114, v116
	v_fma_f32 v126, v114, v114, v117
	v_add_f32_dpp v127, v29, v127 wave_shl:1 row_mask:0xf bank_mask:0xf bound_ctrl:1
	v_pk_add_f32 v[80:81], v[86:87], v[118:119]
	v_pk_add_f32 v[102:103], v[44:45], v[80:81]
	v_pk_add_f32 v[44:45], v[88:89], v[120:121]
	v_pk_add_f32 v[86:87], v[54:55], v[44:45]
	v_pk_add_f32 v[54:55], v[90:91], v[122:123]
	v_pk_add_f32 v[88:89], v[56:57], v[54:55]
	v_pk_add_f32 v[56:57], v[92:93], v[124:125]
	v_pk_add_f32 v[90:91], v[58:59], v[56:57]
	v_pk_add_f32 v[58:59], v[94:95], v[126:127]
	v_pk_add_f32 v[92:93], v[60:61], v[58:59]
	v_mul_f32_e64 v128, v102, v22
	v_mul_f32_e64 v129, v103, v22
	v_mul_f32_e64 v130, v86, v22
	v_fma_f32 v29, v87, v22, v26
	v_mul_f32_e64 v53, v88, v22
	v_mul_f32_e64 v60, v89, v22
	v_fma_f32 v61, v90, v22, v26
	v_mul_f32_e64 v94, v91, v22
	v_fma_f32 v95, v92, v22, v26
	v_fma_f32 v29, -v128, v128, v29
	v_fma_f32 v53, -v128, v129, v53
	v_fma_f32 v60, -v128, v130, v60
	v_fma_f32 v61, -v129, v129, v61
	v_fma_f32 v94, -v129, v130, v94
	v_fma_f32 v95, -v130, v130, v95
	v_mul_f32_e64 v116, v94, v94
	v_mul_f32_e64 v117, v53, v95
	v_mul_f32_e64 v140, v60, v61
	v_mul_f32_e64 v141, v60, v60
	v_mul_f32_e64 v142, v29, v94
	v_mul_f32_e64 v143, v53, v53
	v_fma_f32 v116, v61, v95, -v116
	v_fma_f32 v117, v60, v94, -v117
	v_fma_f32 v140, v53, v94, -v140
	v_fma_f32 v141, v29, v95, -v141
	v_fma_f32 v142, v53, v60, -v142
	v_fma_f32 v143, v29, v61, -v143
	v_mul_f32_e64 v144, v29, v116
	v_fma_f32 v144, v53, v117, v144
	v_fma_f32 v144, v60, v140, v144
	v_rcp_f32_e32 v144, v144
	v_cmp_ne_u32_e64 vcc, s37, v2
	v_mul_f32_e64 v144, v144, v22
	v_cndmask_b32_e64 v144, 0, v144, s[30:31]
	v_cndmask_b32_e64 v29, 0, v18, vcc
	v_cndmask_b32_e64 v137, 0, v22, s[30:31]
	v_mul_f32_e64 v131, v116, v144
	v_mul_f32_e64 v132, v117, v144
	v_mul_f32_e64 v133, v140, v144
	v_mul_f32_e64 v134, v141, v144
	v_mul_f32_e64 v135, v142, v144
	v_mul_f32_e64 v136, v143, v144
	v_add_f32_e64 v138, v93, v29
	v_mov_b32_e32 v139, v2
	ds_write_b128 v23, v[128:131]
	ds_write_b128 v23, v[132:135] offset:1024
	ds_write_b128 v23, v[136:139] offset:2048
	v_mov_b32_dpp v60, v20 wave_shr:1 row_mask:0xf bank_mask:0xf bound_ctrl:1
	v_mov_b32_dpp v61, v21 wave_shr:1 row_mask:0xf bank_mask:0xf bound_ctrl:1
	v_mov_b32_dpp v86, v20 wave_shl:1 row_mask:0xf bank_mask:0xf bound_ctrl:1
	v_mov_b32_dpp v87, v21 wave_shl:1 row_mask:0xf bank_mask:0xf bound_ctrl:1
	v_pk_mul_f32 v[88:89], v[20:21], v[32:33] op_sel_hi:[1,0]
	v_pk_mul_f32 v[90:91], v[20:21], v[32:33] op_sel:[0,1]
	v_pk_mul_f32 v[92:93], v[20:21], v[34:35] op_sel_hi:[1,0]
	v_pk_add_f32 v[94:95], v[20:21], v[60:61]
	v_pk_fma_f32 v[88:89], v[60:61], v[108:109], v[88:89] op_sel_hi:[1,0,1]
	v_pk_fma_f32 v[90:91], v[60:61], v[108:109], v[90:91] op_sel:[0,1,0]
	v_pk_fma_f32 v[92:93], v[60:61], v[110:111], v[92:93] op_sel_hi:[1,0,1]
	v_pk_add_f32 v[94:95], v[94:95], v[86:87]
	v_pk_fma_f32 v[88:89], v[86:87], v[112:113], v[88:89] op_sel_hi:[1,0,1]
	v_pk_fma_f32 v[90:91], v[86:87], v[112:113], v[90:91] op_sel:[0,1,0]
	v_pk_fma_f32 v[92:93], v[86:87], v[114:115], v[92:93] op_sel_hi:[1,0,1]
	s_waitcnt lgkmcnt(0)
	s_barrier
	v_pk_add_f32 v[60:61], v[100:101], v[94:95]
	v_pk_add_f32 v[86:87], v[66:67], v[60:61]
	v_pk_add_f32 v[66:67], v[82:83], v[88:89]
	v_pk_add_f32 v[100:101], v[50:51], v[66:67]
	v_pk_add_f32 v[50:51], v[96:97], v[90:91]
	v_pk_add_f32 v[82:83], v[62:63], v[50:51]
	v_pk_add_f32 v[62:63], v[98:99], v[92:93]
	v_pk_add_f32 v[96:97], v[64:65], v[62:63]
	v_pk_fma_f32 v[100:101], v[128:129], v[86:87], v[100:101] op_sel_hi:[0,1,1] neg_lo:[1,0,0] neg_hi:[1,0,0]
	v_pk_fma_f32 v[82:83], v[128:129], v[86:87], v[82:83] op_sel:[1,0,0] neg_lo:[1,0,0] neg_hi:[1,0,0]
	v_pk_fma_f32 v[96:97], v[130:131], v[86:87], v[96:97] op_sel_hi:[0,1,1] neg_lo:[1,0,0] neg_hi:[1,0,0]
	v_pk_mul_f32 v[64:65], v[130:131], v[100:101] op_sel:[1,0]
	v_pk_mul_f32 v[98:99], v[132:133], v[100:101] op_sel_hi:[0,1]
	v_pk_mul_f32 v[102:103], v[132:133], v[100:101] op_sel:[1,0]
	v_pk_fma_f32 v[64:65], v[132:133], v[82:83], v[64:65] op_sel_hi:[0,1,1]
	v_pk_fma_f32 v[98:99], v[134:135], v[82:83], v[98:99] op_sel_hi:[0,1,1]
	v_pk_fma_f32 v[102:103], v[134:135], v[82:83], v[102:103] op_sel:[1,0,0]
	v_pk_fma_f32 v[64:65], v[132:133], v[96:97], v[64:65] op_sel:[1,0,0]
	v_pk_fma_f32 v[98:99], v[134:135], v[96:97], v[98:99] op_sel:[1,0,0]
	v_pk_fma_f32 v[102:103], v[136:137], v[96:97], v[102:103] op_sel_hi:[0,1,1]
	v_pk_mul_f32 v[116:117], v[128:129], v[64:65] op_sel_hi:[0,1]
	v_pk_fma_f32 v[116:117], v[128:129], v[98:99], v[116:117] op_sel:[1,0,0]
	v_pk_fma_f32 v[116:117], v[130:131], v[102:103], v[116:117] op_sel_hi:[0,1,1]
	v_pk_fma_f32 v[116:117], v[136:137], v[86:87], v[116:117] op_sel:[1,0,0] neg_lo:[0,0,1] neg_hi:[0,0,1]
	s_add_i32 s5, s34, 3
	s_min_i32 s5, s5, 0x200
	s_mul_i32 s6, s5, 0x804
	s_add_i32 s6, s6, s35
	s_add_i32 s7, s6, 0x505014
	s_add_i32 s8, s6, 0x606018
	s_mul_i32 s9, s5, 0x180c
	s_add_i32 s9, s9, s33
	s_add_i32 s4, s34, 4
	s_min_i32 s4, s4, 0x200
	s_mul_i32 s4, s4, 0x804
	s_add_i32 s4, s4, s38
	buffer_load_dword v2, v28, s[20:23], s4 offen nt
	buffer_load_dwordx3 v[8:10], v27, s[24:27], s9 offen nt
	buffer_load_dword v4, v28, s[16:19], s7 offen nt
	buffer_load_dword v5, v28, s[16:19], s8 offen nt
	s_waitcnt vmcnt(8)
	v_mov_b32_dpp v36, v68 wave_shr:1 row_mask:0xf bank_mask:0xf bound_ctrl:1
	v_mov_b32_dpp v37, v69 wave_shr:1 row_mask:0xf bank_mask:0xf bound_ctrl:1
	v_mov_b32_dpp v38, v70 wave_shr:1 row_mask:0xf bank_mask:0xf bound_ctrl:1
	v_mov_b32_dpp v40, v68 wave_shl:1 row_mask:0xf bank_mask:0xf bound_ctrl:1
	v_mov_b32_dpp v41, v69 wave_shl:1 row_mask:0xf bank_mask:0xf bound_ctrl:1
	v_mov_b32_dpp v42, v70 wave_shl:1 row_mask:0xf bank_mask:0xf bound_ctrl:1
	s_add_i32 s4, s34, 2
	s_cmpk_lt_u32 s4, 0x201
	s_cselect_b64 s[12:13], s[40:41], 0
	v_cmp_eq_u32_e64 s[14:15], s37, v24
	s_and_b64 s[14:15], s[14:15], s[12:13]
	v_cndmask_b32_e64 v25, 0, 1, s[14:15]
	v_mul_f32_e64 v82, v68, v68
	v_mul_f32_e64 v83, v68, v69
	v_or_b32_dpp v29, v25, v25 wave_shr:1 row_mask:0xf bank_mask:0xf bound_ctrl:1
	v_mul_f32_e64 v86, v68, v70
	v_or_b32_dpp v29, v25, v29 wave_shl:1 row_mask:0xf bank_mask:0xf bound_ctrl:1
	v_mul_f32_e64 v87, v69, v69
	v_mul_f32_e64 v96, v69, v70
	v_or_b32_dpp v53, v29, v29 wave_shr:1 row_mask:0xf bank_mask:0xf bound_ctrl:1
	v_mul_f32_e64 v97, v70, v70
	s_nop 0
	v_or_b32_dpp v53, v29, v53 wave_shl:1 row_mask:0xf bank_mask:0xf bound_ctrl:1
	v_or3_b32 v25, v53, v84, v85
	v_or3_b32 v25, v25, v52, v30
	s_add_i32 s4, s34, -1
	s_cmpk_lt_u32 s4, 0x1ff
	s_cselect_b64 s[12:13], s[42:43], 0
	v_cmp_ne_u32_e64 s[30:31], 0, v25
	s_and_b64 s[30:31], s[30:31], s[12:13]
	v_cndmask_b32_e64 v25, 0, 1.0, s[30:31]
	v_add_f32_e64 v100, v68, v36
	v_add_f32_e64 v101, v69, v37
	v_add_f32_e64 v128, v70, v38
	v_fma_f32 v82, v36, v36, v82
	v_fma_f32 v83, v36, v37, v83
	v_fma_f32 v86, v36, v38, v86
	v_fma_f32 v87, v37, v37, v87
	v_fma_f32 v96, v37, v38, v96
	v_fma_f32 v97, v38, v38, v97
	v_add_f32_dpp v135, v25, v25 wave_shr:1 row_mask:0xf bank_mask:0xf bound_ctrl:1
	v_add_f32_e64 v100, v100, v40
	v_add_f32_e64 v101, v101, v41
	v_add_f32_e64 v128, v128, v42
	v_fma_f32 v129, v40, v40, v82
	v_fma_f32 v130, v40, v41, v83
	v_fma_f32 v131, v40, v42, v86
	v_fma_f32 v132, v41, v41, v87
	v_fma_f32 v133, v41, v42, v96
	v_fma_f32 v134, v42, v42, v97
	v_add_f32_dpp v135, v25, v135 wave_shl:1 row_mask:0xf bank_mask:0xf bound_ctrl:1
	v_pk_add_f32 v[82:83], v[80:81], v[100:101]
	v_pk_add_f32 v[80:81], v[44:45], v[128:129]
	v_pk_add_f32 v[44:45], v[54:55], v[130:131]
	v_pk_add_f32 v[54:55], v[56:57], v[132:133]
	v_pk_add_f32 v[56:57], v[58:59], v[134:135]
	v_mul_f32_e64 v136, v82, v22
	v_mul_f32_e64 v137, v83, v22
	v_mul_f32_e64 v138, v80, v22
	v_fma_f32 v25, v81, v22, v26
	v_mul_f32_e64 v29, v44, v22
	v_mul_f32_e64 v58, v45, v22
	v_fma_f32 v59, v54, v22, v26
	v_mul_f32_e64 v86, v55, v22
	v_fma_f32 v87, v56, v22, v26
	v_fma_f32 v25, -v136, v136, v25
	v_fma_f32 v29, -v136, v137, v29
	v_fma_f32 v58, -v136, v138, v58
	v_fma_f32 v59, -v137, v137, v59
	v_fma_f32 v86, -v137, v138, v86
	v_fma_f32 v87, -v138, v138, v87
	v_mul_f32_e64 v96, v86, v86
	v_mul_f32_e64 v97, v29, v87
	v_mul_f32_e64 v148, v58, v59
	v_mul_f32_e64 v149, v58, v58
	v_mul_f32_e64 v150, v25, v86
	v_mul_f32_e64 v151, v29, v29
	v_fma_f32 v96, v59, v87, -v96
	v_fma_f32 v97, v58, v86, -v97
	v_fma_f32 v148, v29, v86, -v148
	v_fma_f32 v149, v25, v87, -v149
	v_fma_f32 v150, v29, v58, -v150
	v_fma_f32 v151, v25, v59, -v151
	v_mul_f32_e64 v152, v25, v96
	v_fma_f32 v152, v29, v97, v152
	v_fma_f32 v152, v58, v148, v152
	v_rcp_f32_e32 v152, v152
	v_cmp_ne_u32_e64 vcc, s37, v3
	v_mul_f32_e64 v152, v152, v22
	v_cndmask_b32_e64 v152, 0, v152, s[30:31]
	v_cndmask_b32_e64 v25, 0, v18, vcc
	v_cndmask_b32_e64 v145, 0, v22, s[30:31]
	v_mul_f32_e64 v139, v96, v152
	v_mul_f32_e64 v140, v97, v152
	v_mul_f32_e64 v141, v148, v152
	v_mul_f32_e64 v142, v149, v152
	v_mul_f32_e64 v143, v150, v152
	v_mul_f32_e64 v144, v151, v152
	v_add_f32_e64 v146, v57, v25
	v_mov_b32_e32 v147, v3
	ds_write_b128 v23, v[136:139] offset:3072
	ds_write_b128 v23, v[140:143] offset:4096
	ds_write_b128 v23, v[144:147] offset:5120
	v_mov_b32_dpp v44, v46 wave_shr:1 row_mask:0xf bank_mask:0xf bound_ctrl:1
	v_mov_b32_dpp v45, v47 wave_shr:1 row_mask:0xf bank_mask:0xf bound_ctrl:1
	v_mov_b32_dpp v54, v46 wave_shl:1 row_mask:0xf bank_mask:0xf bound_ctrl:1
	v_mov_b32_dpp v55, v47 wave_shl:1 row_mask:0xf bank_mask:0xf bound_ctrl:1
	v_pk_mul_f32 v[56:57], v[46:47], v[68:69] op_sel_hi:[1,0]
	v_pk_mul_f32 v[58:59], v[46:47], v[68:69] op_sel:[0,1]
	v_pk_mul_f32 v[80:81], v[46:47], v[70:71] op_sel_hi:[1,0]
	v_pk_add_f32 v[82:83], v[46:47], v[44:45]
	v_pk_fma_f32 v[56:57], v[44:45], v[36:37], v[56:57] op_sel_hi:[1,0,1]
	v_pk_fma_f32 v[58:59], v[44:45], v[36:37], v[58:59] op_sel:[0,1,0]
	v_pk_fma_f32 v[80:81], v[44:45], v[38:39], v[80:81] op_sel_hi:[1,0,1]
	v_pk_add_f32 v[82:83], v[82:83], v[54:55]
	v_pk_fma_f32 v[56:57], v[54:55], v[40:41], v[56:57] op_sel_hi:[1,0,1]
	v_pk_fma_f32 v[58:59], v[54:55], v[40:41], v[58:59] op_sel:[0,1,0]
	v_pk_fma_f32 v[80:81], v[54:55], v[42:43], v[80:81] op_sel_hi:[1,0,1]
	s_waitcnt lgkmcnt(0)
	s_barrier
	v_pk_add_f32 v[44:45], v[60:61], v[82:83]
	v_pk_add_f32 v[54:55], v[66:67], v[56:57]
	v_pk_add_f32 v[60:61], v[50:51], v[58:59]
	v_pk_add_f32 v[50:51], v[62:63], v[80:81]
	v_pk_fma_f32 v[54:55], v[136:137], v[44:45], v[54:55] op_sel_hi:[0,1,1] neg_lo:[1,0,0] neg_hi:[1,0,0]
	v_pk_fma_f32 v[60:61], v[136:137], v[44:45], v[60:61] op_sel:[1,0,0] neg_lo:[1,0,0] neg_hi:[1,0,0]
	v_pk_fma_f32 v[50:51], v[138:139], v[44:45], v[50:51] op_sel_hi:[0,1,1] neg_lo:[1,0,0] neg_hi:[1,0,0]
	v_pk_mul_f32 v[62:63], v[138:139], v[54:55] op_sel:[1,0]
	v_pk_mul_f32 v[66:67], v[140:141], v[54:55] op_sel_hi:[0,1]
	v_pk_mul_f32 v[86:87], v[140:141], v[54:55] op_sel:[1,0]
	v_pk_fma_f32 v[62:63], v[140:141], v[60:61], v[62:63] op_sel_hi:[0,1,1]
	v_pk_fma_f32 v[66:67], v[142:143], v[60:61], v[66:67] op_sel_hi:[0,1,1]
	v_pk_fma_f32 v[86:87], v[142:143], v[60:61], v[86:87] op_sel:[1,0,0]
	v_pk_fma_f32 v[62:63], v[140:141], v[50:51], v[62:63] op_sel:[1,0,0]
	v_pk_fma_f32 v[66:67], v[142:143], v[50:51], v[66:67] op_sel:[1,0,0]
	v_pk_fma_f32 v[86:87], v[144:145], v[50:51], v[86:87] op_sel_hi:[0,1,1]
	v_pk_mul_f32 v[96:97], v[136:137], v[62:63] op_sel_hi:[0,1]
	v_pk_fma_f32 v[96:97], v[136:137], v[66:67], v[96:97] op_sel:[1,0,0]
	v_pk_fma_f32 v[96:97], v[138:139], v[86:87], v[96:97] op_sel_hi:[0,1,1]
	v_pk_fma_f32 v[96:97], v[144:145], v[44:45], v[96:97] op_sel:[1,0,0] neg_lo:[0,0,1] neg_hi:[0,0,1]
	s_add_i32 s5, s34, 4
	s_min_i32 s5, s5, 0x200
	s_mul_i32 s6, s5, 0x804
	s_add_i32 s6, s6, s35
	s_add_i32 s7, s6, 0x505014
	s_add_i32 s8, s6, 0x606018
	s_mul_i32 s9, s5, 0x180c
	s_add_i32 s9, s9, s33
	s_add_i32 s4, s34, 5
	s_min_i32 s4, s4, 0x200
	s_mul_i32 s4, s4, 0x804
	s_add_i32 s4, s4, s38
	buffer_load_dword v3, v28, s[20:23], s4 offen nt
	buffer_load_dwordx3 v[12:14], v27, s[24:27], s9 offen nt
	buffer_load_dword v6, v28, s[16:19], s7 offen nt
	buffer_load_dword v7, v28, s[16:19], s8 offen nt
	s_waitcnt vmcnt(8)
	v_mov_b32_dpp v72, v104 wave_shr:1 row_mask:0xf bank_mask:0xf bound_ctrl:1
	v_mov_b32_dpp v73, v105 wave_shr:1 row_mask:0xf bank_mask:0xf bound_ctrl:1
	v_mov_b32_dpp v74, v106 wave_shr:1 row_mask:0xf bank_mask:0xf bound_ctrl:1
	v_mov_b32_dpp v76, v104 wave_shl:1 row_mask:0xf bank_mask:0xf bound_ctrl:1
	v_mov_b32_dpp v77, v105 wave_shl:1 row_mask:0xf bank_mask:0xf bound_ctrl:1
	v_mov_b32_dpp v78, v106 wave_shl:1 row_mask:0xf bank_mask:0xf bound_ctrl:1
	s_add_i32 s4, s34, 3
	s_cmpk_lt_u32 s4, 0x201
	s_cselect_b64 s[12:13], s[40:41], 0
	v_cmp_eq_u32_e64 s[14:15], s37, v17
	s_and_b64 s[14:15], s[14:15], s[12:13]
	v_cndmask_b32_e64 v25, 0, 1, s[14:15]
	v_mul_f32_e64 v44, v104, v104
	v_mul_f32_e64 v45, v104, v105
	v_or_b32_dpp v29, v25, v25 wave_shr:1 row_mask:0xf bank_mask:0xf bound_ctrl:1
	v_mul_f32_e64 v50, v104, v106
	v_or_b32_dpp v29, v25, v29 wave_shl:1 row_mask:0xf bank_mask:0xf bound_ctrl:1
	v_mul_f32_e64 v51, v105, v105
	v_mul_f32_e64 v54, v105, v106
	v_or_b32_dpp v30, v29, v29 wave_shr:1 row_mask:0xf bank_mask:0xf bound_ctrl:1
	v_mul_f32_e64 v55, v106, v106
	s_nop 0
	v_or_b32_dpp v30, v29, v30 wave_shl:1 row_mask:0xf bank_mask:0xf bound_ctrl:1
	v_or3_b32 v25, v30, v53, v84
	v_or3_b32 v25, v25, v85, v52
	s_add_i32 s4, s34, 0
	s_cmpk_lt_u32 s4, 0x1ff
	s_cselect_b64 s[12:13], s[42:43], 0
	v_cmp_ne_u32_e64 s[30:31], 0, v25
	s_and_b64 s[30:31], s[30:31], s[12:13]
	v_cndmask_b32_e64 v25, 0, 1.0, s[30:31]
	v_add_f32_e64 v60, v104, v72
	v_add_f32_e64 v61, v105, v73
	v_add_f32_e64 v136, v106, v74
	v_fma_f32 v44, v72, v72, v44
	v_fma_f32 v45, v72, v73, v45
	v_fma_f32 v50, v72, v74, v50
	v_fma_f32 v51, v73, v73, v51
	v_fma_f32 v54, v73, v74, v54
	v_fma_f32 v55, v74, v74, v55
	v_add_f32_dpp v143, v25, v25 wave_shr:1 row_mask:0xf bank_mask:0xf bound_ctrl:1
	v_add_f32_e64 v60, v60, v76
	v_add_f32_e64 v61, v61, v77
	v_add_f32_e64 v136, v136, v78
	v_fma_f32 v137, v76, v76, v44
	v_fma_f32 v138, v76, v77, v45
	v_fma_f32 v139, v76, v78, v50
	v_fma_f32 v140, v77, v77, v51
	v_fma_f32 v141, v77, v78, v54
	v_fma_f32 v142, v78, v78, v55
	v_add_f32_dpp v143, v25, v143 wave_shl:1 row_mask:0xf bank_mask:0xf bound_ctrl:1
	v_pk_add_f32 v[44:45], v[100:101], v[60:61]
	v_pk_add_f32 v[50:51], v[118:119], v[44:45]
	v_pk_add_f32 v[54:55], v[128:129], v[136:137]
	v_pk_add_f32 v[100:101], v[120:121], v[54:55]
	v_pk_add_f32 v[118:119], v[130:131], v[138:139]
	v_pk_add_f32 v[120:121], v[122:123], v[118:119]
	v_pk_add_f32 v[122:123], v[132:133], v[140:141]
	v_pk_add_f32 v[128:129], v[124:125], v[122:123]
	v_pk_add_f32 v[124:125], v[134:135], v[142:143]
	v_pk_add_f32 v[130:131], v[126:127], v[124:125]
	v_mul_f32_e64 v132, v50, v22
	v_mul_f32_e64 v133, v51, v22
	v_mul_f32_e64 v134, v100, v22
	v_fma_f32 v25, v101, v22, v26
	v_mul_f32_e64 v29, v120, v22
	v_mul_f32_e64 v126, v121, v22
	v_fma_f32 v127, v128, v22, v26
	v_mul_f32_e64 v152, v129, v22
	v_fma_f32 v153, v130, v22, v26
	v_fma_f32 v25, -v132, v132, v25
	v_fma_f32 v29, -v132, v133, v29
	v_fma_f32 v126, -v132, v134, v126
	v_fma_f32 v127, -v133, v133, v127
	v_fma_f32 v152, -v133, v134, v152
	v_fma_f32 v153, -v134, v134, v153
	v_mul_f32_e64 v154, v152, v152
	v_mul_f32_e64 v155, v29, v153
	v_mul_f32_e64 v156, v126, v127
	v_mul_f32_e64 v157, v126, v126
	v_mul_f32_e64 v158, v25, v152
	v_mul_f32_e64 v159, v29, v29
	v_fma_f32 v154, v127, v153, -v154
	v_fma_f32 v155, v126, v152, -v155
	v_fma_f32 v156, v29, v152, -v156
	v_fma_f32 v157, v25, v153, -v157
	v_fma_f32 v158, v29, v126, -v158
	v_fma_f32 v159, v25, v127, -v159
	v_mul_f32_e64 v160, v25, v154
	v_fma_f32 v160, v29, v155, v160
	v_fma_f32 v160, v126, v156, v160
	v_rcp_f32_e32 v160, v160
	v_cmp_ne_u32_e64 vcc, s37, v16
	v_mul_f32_e64 v160, v160, v22
	v_cndmask_b32_e64 v160, 0, v160, s[30:31]
	v_cndmask_b32_e64 v25, 0, v18, vcc
	v_cndmask_b32_e64 v149, 0, v22, s[30:31]
	v_mul_f32_e64 v135, v154, v160
	v_mul_f32_e64 v144, v155, v160
	v_mul_f32_e64 v145, v156, v160
	v_mul_f32_e64 v146, v157, v160
	v_mul_f32_e64 v147, v158, v160
	v_mul_f32_e64 v148, v159, v160
	v_add_f32_e64 v150, v131, v25
	v_mov_b32_e32 v151, v16
	ds_write_b128 v23, v[132:135]
	ds_write_b128 v23, v[144:147] offset:1024
	ds_write_b128 v23, v[148:151] offset:2048
	v_mov_b32_dpp v50, v48 wave_shr:1 row_mask:0xf bank_mask:0xf bound_ctrl:1
	v_mov_b32_dpp v51, v49 wave_shr:1 row_mask:0xf bank_mask:0xf bound_ctrl:1
	v_mov_b32_dpp v100, v48 wave_shl:1 row_mask:0xf bank_mask:0xf bound_ctrl:1
	v_mov_b32_dpp v101, v49 wave_shl:1 row_mask:0xf bank_mask:0xf bound_ctrl:1
	v_pk_mul_f32 v[120:121], v[48:49], v[104:105] op_sel_hi:[1,0]
	v_pk_mul_f32 v[126:127], v[48:49], v[104:105] op_sel:[0,1]
	v_pk_mul_f32 v[128:129], v[48:49], v[106:107] op_sel_hi:[1,0]
	v_pk_add_f32 v[130:131], v[48:49], v[50:51]
	v_pk_fma_f32 v[120:121], v[50:51], v[72:73], v[120:121] op_sel_hi:[1,0,1]
	v_pk_fma_f32 v[126:127], v[50:51], v[72:73], v[126:127] op_sel:[0,1,0]
	v_pk_fma_f32 v[128:129], v[50:51], v[74:75], v[128:129] op_sel_hi:[1,0,1]
	v_pk_add_f32 v[130:131], v[130:131], v[100:101]
	v_pk_fma_f32 v[120:121], v[100:101], v[76:77], v[120:121] op_sel_hi:[1,0,1]
	v_pk_fma_f32 v[126:127], v[100:101], v[76:77], v[126:127] op_sel:[0,1,0]
	v_pk_fma_f32 v[128:129], v[100:101], v[78:79], v[128:129] op_sel_hi:[1,0,1]
	s_waitcnt lgkmcnt(0)
	s_barrier
	v_pk_add_f32 v[50:51], v[82:83], v[130:131]
	v_pk_add_f32 v[100:101], v[94:95], v[50:51]
	v_pk_add_f32 v[82:83], v[56:57], v[120:121]
	v_pk_add_f32 v[94:95], v[88:89], v[82:83]
	v_pk_add_f32 v[56:57], v[58:59], v[126:127]
	v_pk_add_f32 v[88:89], v[90:91], v[56:57]
	v_pk_add_f32 v[58:59], v[80:81], v[128:129]
	v_pk_add_f32 v[90:91], v[92:93], v[58:59]
	v_pk_fma_f32 v[94:95], v[132:133], v[100:101], v[94:95] op_sel_hi:[0,1,1] neg_lo:[1,0,0] neg_hi:[1,0,0]
	v_pk_fma_f32 v[88:89], v[132:133], v[100:101], v[88:89] op_sel:[1,0,0] neg_lo:[1,0,0] neg_hi:[1,0,0]
	v_pk_fma_f32 v[90:91], v[134:135], v[100:101], v[90:91] op_sel_hi:[0,1,1] neg_lo:[1,0,0] neg_hi:[1,0,0]
	v_pk_mul_f32 v[80:81], v[134:135], v[94:95] op_sel:[1,0]
	v_pk_mul_f32 v[92:93], v[144:145], v[94:95] op_sel_hi:[0,1]
	v_pk_mul_f32 v[152:153], v[144:145], v[94:95] op_sel:[1,0]
	v_pk_fma_f32 v[80:81], v[144:145], v[88:89], v[80:81] op_sel_hi:[0,1,1]
	v_pk_fma_f32 v[92:93], v[146:147], v[88:89], v[92:93] op_sel_hi:[0,1,1]
	v_pk_fma_f32 v[152:153], v[146:147], v[88:89], v[152:153] op_sel:[1,0,0]
	v_pk_fma_f32 v[80:81], v[144:145], v[90:91], v[80:81] op_sel:[1,0,0]
	v_pk_fma_f32 v[92:93], v[146:147], v[90:91], v[92:93] op_sel:[1,0,0]
	v_pk_fma_f32 v[152:153], v[148:149], v[90:91], v[152:153] op_sel_hi:[0,1,1]
	v_pk_mul_f32 v[154:155], v[132:133], v[80:81] op_sel_hi:[0,1]
	v_pk_fma_f32 v[154:155], v[132:133], v[92:93], v[154:155] op_sel:[1,0,0]
	v_pk_fma_f32 v[154:155], v[134:135], v[152:153], v[154:155] op_sel_hi:[0,1,1]
	v_pk_fma_f32 v[154:155], v[148:149], v[100:101], v[154:155] op_sel:[1,0,0] neg_lo:[0,0,1] neg_hi:[0,0,1]
	v_cmp_eq_u32_e64 s[10:11], 6, v151
	v_cmp_eq_u32_e64 s[14:15], 7, v151
	v_pk_add_f32 v[88:89], v[62:63], v[80:81]
	v_pk_add_f32 v[90:91], v[64:65], v[88:89]
	v_pk_add_f32 v[62:63], v[66:67], v[92:93]
	v_pk_add_f32 v[64:65], v[98:99], v[62:63]
	v_pk_add_f32 v[66:67], v[86:87], v[152:153]
	v_pk_add_f32 v[94:95], v[102:103], v[66:67]
	v_pk_add_f32 v[86:87], v[96:97], v[154:155]
	v_pk_add_f32 v[98:99], v[116:117], v[86:87]
	v_pk_fma_f32 v[96:97], v[108:109], v[90:91], v[98:99] op_sel_hi:[0,1,1]
	v_pk_fma_f32 v[100:101], v[112:113], v[90:91], v[98:99] op_sel_hi:[0,1,1]
	v_pk_fma_f32 v[96:97], v[108:109], v[64:65], v[96:97] op_sel:[1,0,0]
	v_pk_fma_f32 v[100:101], v[112:113], v[64:65], v[100:101] op_sel:[1,0,0]
	v_pk_fma_f32 v[96:97], v[110:111], v[94:95], v[96:97] op_sel_hi:[0,1,1]
	v_pk_fma_f32 v[100:101], v[114:115], v[94:95], v[100:101] op_sel_hi:[0,1,1]
	v_pk_fma_f32 v[98:99], v[32:33], v[90:91], v[98:99] op_sel_hi:[0,1,1]
	v_pk_fma_f32 v[98:99], v[32:33], v[64:65], v[98:99] op_sel:[1,0,0]
	v_pk_fma_f32 v[98:99], v[34:35], v[94:95], v[98:99] op_sel_hi:[0,1,1]
	v_cndmask_b32_e64 v102, 0, v18, s[10:11]
	v_cndmask_b32_e64 v103, 0, v18, s[14:15]
	v_add_f32_dpp v98, v96, v98 wave_shl:1 row_mask:0xf bank_mask:0xf bound_ctrl:1
	v_add_f32_dpp v99, v97, v99 wave_shl:1 row_mask:0xf bank_mask:0xf bound_ctrl:1
	s_add_i32 s4, s34, 0
	s_cmpk_lt_i32 s4, 0x201
	s_cselect_b64 s[12:13], s[0:1], 0
	v_add_f32_dpp v98, v100, v98 wave_shr:1 row_mask:0xf bank_mask:0xf bound_ctrl:1
	v_add_f32_dpp v99, v101, v99 wave_shr:1 row_mask:0xf bank_mask:0xf bound_ctrl:1
	v_pk_fma_f32 v[98:99], v[20:21], v[150:151], v[98:99] op_sel_hi:[1,0,1] neg_lo:[0,0,1] neg_hi:[0,0,1]
	v_pk_add_f32 v[98:99], v[98:99], v[102:103] neg_lo:[0,1] neg_hi:[0,1]
	v_pk_mul_f32 v[116:117], v[98:99], v[98:99]
	v_add_f32_e32 v116, v116, v117
	v_cndmask_b32_e64 v117, 0, v116, s[12:13]
	v_add_f32_e32 v1, v1, v117
	s_add_i32 s5, s34, 5
	s_min_i32 s5, s5, 0x200
	s_mul_i32 s6, s5, 0x804
	s_add_i32 s6, s6, s35
	s_add_i32 s7, s6, 0x505014
	s_add_i32 s8, s6, 0x606018
	s_mul_i32 s9, s5, 0x180c
	s_add_i32 s9, s9, s33
	s_add_i32 s4, s34, 6
	s_min_i32 s4, s4, 0x200
	s_mul_i32 s4, s4, 0x804
	s_add_i32 s4, s4, s38
	buffer_load_dword v16, v28, s[20:23], s4 offen nt
	buffer_load_dwordx3 v[32:34], v27, s[24:27], s9 offen nt
	buffer_load_dword v20, v28, s[16:19], s7 offen nt
	buffer_load_dword v21, v28, s[16:19], s8 offen nt
	s_waitcnt vmcnt(8)
	v_mov_b32_dpp v96, v8 wave_shr:1 row_mask:0xf bank_mask:0xf bound_ctrl:1
	v_mov_b32_dpp v97, v9 wave_shr:1 row_mask:0xf bank_mask:0xf bound_ctrl:1
	v_mov_b32_dpp v98, v10 wave_shr:1 row_mask:0xf bank_mask:0xf bound_ctrl:1
	v_mov_b32_dpp v100, v8 wave_shl:1 row_mask:0xf bank_mask:0xf bound_ctrl:1
	v_mov_b32_dpp v101, v9 wave_shl:1 row_mask:0xf bank_mask:0xf bound_ctrl:1
	v_mov_b32_dpp v102, v10 wave_shl:1 row_mask:0xf bank_mask:0xf bound_ctrl:1
	s_add_i32 s4, s34, 4
	s_cmpk_lt_u32 s4, 0x201
	s_cselect_b64 s[12:13], s[40:41], 0
	v_cmp_eq_u32_e64 s[14:15], s37, v2
	s_and_b64 s[14:15], s[14:15], s[12:13]
	v_cndmask_b32_e64 v25, 0, 1, s[14:15]
	v_mul_f32_e64 v64, v8, v8
	v_mul_f32_e64 v65, v8, v9
	v_or_b32_dpp v29, v25, v25 wave_shr:1 row_mask:0xf bank_mask:0xf bound_ctrl:1
	v_mul_f32_e64 v90, v8, v10
	v_or_b32_dpp v29, v25, v29 wave_shl:1 row_mask:0xf bank_mask:0xf bound_ctrl:1
	v_mul_f32_e64 v91, v9, v9
	v_mul_f32_e64 v94, v9, v10
	v_or_b32_dpp v52, v29, v29 wave_shr:1 row_mask:0xf bank_mask:0xf bound_ctrl:1
	v_mul_f32_e64 v95, v10, v10
	s_nop 0
	v_or_b32_dpp v52, v29, v52 wave_shl:1 row_mask:0xf bank_mask:0xf bound_ctrl:1
	v_or3_b32 v25, v52, v30, v53
	v_or3_b32 v25, v25, v84, v85
	s_add_i32 s4, s34, 1
	s_cmpk_lt_u32 s4, 0x1ff
	s_cselect_b64 s[12:13], s[42:43], 0
	v_cmp_ne_u32_e64 s[30:31], 0, v25
	s_and_b64 s[30:31], s[30:31], s[12:13]
	v_cndmask_b32_e64 v25, 0, 1.0, s[30:31]
	v_add_f32_e64 v108, v8, v96
	v_add_f32_e64 v109, v9, v97
	v_add_f32_e64 v110, v10, v98
	v_fma_f32 v64, v96, v96, v64
	v_fma_f32 v65, v96, v97, v65
	v_fma_f32 v90, v96, v98, v90
	v_fma_f32 v91, v97, v97, v91
	v_fma_f32 v94, v97, v98, v94
	v_fma_f32 v95, v98, v98, v95
	v_add_f32_dpp v117, v25, v25 wave_shr:1 row_mask:0xf bank_mask:0xf bound_ctrl:1
	v_add_f32_e64 v108, v108, v100
	v_add_f32_e64 v109, v109, v101
	v_add_f32_e64 v110, v110, v102
	v_fma_f32 v111, v100, v100, v64
	v_fma_f32 v112, v100, v101, v65
	v_fma_f32 v113, v100, v102, v90
	v_fma_f32 v114, v101, v101, v91
	v_fma_f32 v115, v101, v102, v94
	v_fma_f32 v116, v102, v102, v95
	v_add_f32_dpp v117, v25, v117 wave_shl:1 row_mask:0xf bank_mask:0xf bound_ctrl:1
	v_pk_add_f32 v[64:65], v[44:45], v[108:109]
	v_pk_add_f32 v[44:45], v[54:55], v[110:111]
	v_pk_add_f32 v[54:55], v[118:119], v[112:113]
	v_pk_add_f32 v[90:91], v[122:123], v[114:115]
	v_pk_add_f32 v[94:95], v[124:125], v[116:117]
	v_mul_f32_e64 v132, v64, v22
	v_mul_f32_e64 v133, v65, v22
	v_mul_f32_e64 v134, v44, v22
	v_fma_f32 v25, v45, v22, v26
	v_mul_f32_e64 v29, v54, v22
	v_mul_f32_e64 v118, v55, v22
	v_fma_f32 v119, v90, v22, v26
	v_mul_f32_e64 v122, v91, v22
	v_fma_f32 v123, v94, v22, v26
	v_fma_f32 v25, -v132, v132, v25
	v_fma_f32 v29, -v132, v133, v29
	v_fma_f32 v118, -v132, v134, v118
	v_fma_f32 v119, -v133, v133, v119
	v_fma_f32 v122, -v133, v134, v122
	v_fma_f32 v123, -v134, v134, v123
	v_mul_f32_e64 v124, v122, v122
	v_mul_f32_e64 v125, v29, v123
	v_mul_f32_e64 v156, v118, v119
	v_mul_f32_e64 v157, v118, v118
	v_mul_f32_e64 v158, v25, v122
	v_mul_f32_e64 v159, v29, v29
	v_fma_f32 v124, v119, v123, -v124
	v_fma_f32 v125, v118, v122, -v125
	v_fma_f32 v156, v29, v122, -v156
	v_fma_f32 v157, v25, v123, -v157
	v_fma_f32 v158, v29, v118, -v158
	v_fma_f32 v159, v25, v119, -v159
	v_mul_f32_e64 v160, v25, v124
	v_fma_f32 v160, v29, v125, v160
	v_fma_f32 v160, v118, v156, v160
	v_rcp_f32_e32 v160, v160
	v_cmp_ne_u32_e64 vcc, s37, v31
	v_mul_f32_e64 v160, v160, v22
	v_cndmask_b32_e64 v160, 0, v160, s[30:31]
	v_cndmask_b32_e64 v25, 0, v18, vcc
	v_cndmask_b32_e64 v149, 0, v22, s[30:31]
	v_mul_f32_e64 v135, v124, v160
	v_mul_f32_e64 v144, v125, v160
	v_mul_f32_e64 v145, v156, v160
	v_mul_f32_e64 v146, v157, v160
	v_mul_f32_e64 v147, v158, v160
	v_mul_f32_e64 v148, v159, v160
	v_add_f32_e64 v150, v95, v25
	v_mov_b32_e32 v151, v31
	ds_write_b128 v23, v[132:135] offset:3072
	ds_write_b128 v23, v[144:147] offset:4096
	ds_write_b128 v23, v[148:151] offset:5120
	v_mov_b32_dpp v44, v4 wave_shr:1 row_mask:0xf bank_mask:0xf bound_ctrl:1
	v_mov_b32_dpp v45, v5 wave_shr:1 row_mask:0xf bank_mask:0xf bound_ctrl:1
	v_mov_b32_dpp v54, v4 wave_shl:1 row_mask:0xf bank_mask:0xf bound_ctrl:1
	v_mov_b32_dpp v55, v5 wave_shl:1 row_mask:0xf bank_mask:0xf bound_ctrl:1
	v_pk_mul_f32 v[64:65], v[4:5], v[8:9] op_sel_hi:[1,0]
	v_pk_mul_f32 v[90:91], v[4:5], v[8:9] op_sel:[0,1]
	v_pk_mul_f32 v[94:95], v[4:5], v[10:11] op_sel_hi:[1,0]
	v_pk_add_f32 v[118:119], v[4:5], v[44:45]
	v_pk_fma_f32 v[64:65], v[44:45], v[96:97], v[64:65] op_sel_hi:[1,0,1]
	v_pk_fma_f32 v[90:91], v[44:45], v[96:97], v[90:91] op_sel:[0,1,0]
	v_pk_fma_f32 v[94:95], v[44:45], v[98:99], v[94:95] op_sel_hi:[1,0,1]
	v_pk_add_f32 v[118:119], v[118:119], v[54:55]
	v_pk_fma_f32 v[64:65], v[54:55], v[100:101], v[64:65] op_sel_hi:[1,0,1]
	v_pk_fma_f32 v[90:91], v[54:55], v[100:101], v[90:91] op_sel:[0,1,0]
	v_pk_fma_f32 v[94:95], v[54:55], v[102:103], v[94:95] op_sel_hi:[1,0,1]
	s_waitcnt lgkmcnt(0)
	s_barrier
	v_pk_add_f32 v[44:45], v[50:51], v[118:119]
	v_pk_add_f32 v[50:51], v[82:83], v[64:65]
	v_pk_add_f32 v[54:55], v[56:57], v[90:91]
	v_pk_add_f32 v[56:57], v[58:59], v[94:95]
	v_pk_fma_f32 v[50:51], v[132:133], v[44:45], v[50:51] op_sel_hi:[0,1,1] neg_lo:[1,0,0] neg_hi:[1,0,0]
	v_pk_fma_f32 v[54:55], v[132:133], v[44:45], v[54:55] op_sel:[1,0,0] neg_lo:[1,0,0] neg_hi:[1,0,0]
	v_pk_fma_f32 v[56:57], v[134:135], v[44:45], v[56:57] op_sel_hi:[0,1,1] neg_lo:[1,0,0] neg_hi:[1,0,0]
	v_pk_mul_f32 v[58:59], v[134:135], v[50:51] op_sel:[1,0]
	v_pk_mul_f32 v[82:83], v[144:145], v[50:51] op_sel_hi:[0,1]
	v_pk_mul_f32 v[122:123], v[144:145], v[50:51] op_sel:[1,0]
	v_pk_fma_f32 v[58:59], v[144:145], v[54:55], v[58:59] op_sel_hi:[0,1,1]
	v_pk_fma_f32 v[82:83], v[146:147], v[54:55], v[82:83] op_sel_hi:[0,1,1]
	v_pk_fma_f32 v[122:123], v[146:147], v[54:55], v[122:123] op_sel:[1,0,0]
	v_pk_fma_f32 v[58:59], v[144:145], v[56:57], v[58:59] op_sel:[1,0,0]
	v_pk_fma_f32 v[82:83], v[146:147], v[56:57], v[82:83] op_sel:[1,0,0]
	v_pk_fma_f32 v[122:123], v[148:149], v[56:57], v[122:123] op_sel_hi:[0,1,1]
	v_pk_mul_f32 v[124:125], v[132:133], v[58:59] op_sel_hi:[0,1]
	v_pk_fma_f32 v[124:125], v[132:133], v[82:83], v[124:125] op_sel:[1,0,0]
	v_pk_fma_f32 v[124:125], v[134:135], v[122:123], v[124:125] op_sel_hi:[0,1,1]
	v_pk_fma_f32 v[124:125], v[148:149], v[44:45], v[124:125] op_sel:[1,0,0] neg_lo:[0,0,1] neg_hi:[0,0,1]
	v_cmp_eq_u32_e64 s[10:11], 6, v151
	v_cmp_eq_u32_e64 s[14:15], 7, v151
	v_pk_add_f32 v[44:45], v[88:89], v[58:59]
	v_pk_add_f32 v[50:51], v[62:63], v[82:83]
	v_pk_add_f32 v[54:55], v[66:67], v[122:123]
	v_pk_add_f32 v[56:57], v[86:87], v[124:125]
	v_pk_fma_f32 v[62:63], v[36:37], v[44:45], v[56:57] op_sel_hi:[0,1,1]
	v_pk_fma_f32 v[66:67], v[40:41], v[44:45], v[56:57] op_sel_hi:[0,1,1]
	v_pk_fma_f32 v[62:63], v[36:37], v[50:51], v[62:63] op_sel:[1,0,0]
	v_pk_fma_f32 v[66:67], v[40:41], v[50:51], v[66:67] op_sel:[1,0,0]
	v_pk_fma_f32 v[62:63], v[38:39], v[54:55], v[62:63] op_sel_hi:[0,1,1]
	v_pk_fma_f32 v[66:67], v[42:43], v[54:55], v[66:67] op_sel_hi:[0,1,1]
	v_pk_fma_f32 v[56:57], v[68:69], v[44:45], v[56:57] op_sel_hi:[0,1,1]
	v_pk_fma_f32 v[56:57], v[68:69], v[50:51], v[56:57] op_sel:[1,0,0]
	v_pk_fma_f32 v[56:57], v[70:71], v[54:55], v[56:57] op_sel_hi:[0,1,1]
	v_cndmask_b32_e64 v86, 0, v18, s[10:11]
	v_cndmask_b32_e64 v87, 0, v18, s[14:15]
	v_add_f32_dpp v56, v62, v56 wave_shl:1 row_mask:0xf bank_mask:0xf bound_ctrl:1
	v_add_f32_dpp v57, v63, v57 wave_shl:1 row_mask:0xf bank_mask:0xf bound_ctrl:1
	s_add_i32 s4, s34, 1
	s_cmpk_lt_i32 s4, 0x201
	s_cselect_b64 s[12:13], s[0:1], 0
	v_add_f32_dpp v56, v66, v56 wave_shr:1 row_mask:0xf bank_mask:0xf bound_ctrl:1
	v_add_f32_dpp v57, v67, v57 wave_shr:1 row_mask:0xf bank_mask:0xf bound_ctrl:1
	v_pk_fma_f32 v[56:57], v[46:47], v[150:151], v[56:57] op_sel_hi:[1,0,1] neg_lo:[0,0,1] neg_hi:[0,0,1]
	v_pk_add_f32 v[56:57], v[56:57], v[86:87] neg_lo:[0,1] neg_hi:[0,1]
	v_pk_mul_f32 v[88:89], v[56:57], v[56:57]
	v_add_f32_e32 v88, v88, v89
	v_cndmask_b32_e64 v89, 0, v88, s[12:13]
	v_add_f32_e32 v1, v1, v89
	s_add_i32 s5, s34, 6
	s_min_i32 s5, s5, 0x200
	s_mul_i32 s6, s5, 0x804
	s_add_i32 s6, s6, s35
	s_add_i32 s7, s6, 0x505014
	s_add_i32 s8, s6, 0x606018
	s_mul_i32 s9, s5, 0x180c
	s_add_i32 s9, s9, s33
	s_add_i32 s4, s34, 7
	s_min_i32 s4, s4, 0x200
	s_mul_i32 s4, s4, 0x804
	s_add_i32 s4, s4, s38
	buffer_load_dword v25, v28, s[20:23], s4 offen nt
	buffer_load_dwordx3 v[40:42], v27, s[24:27], s9 offen nt
	buffer_load_dword v36, v28, s[16:19], s7 offen nt
	buffer_load_dword v37, v28, s[16:19], s8 offen nt
	s_waitcnt vmcnt(8)
	v_mov_b32_dpp v44, v12 wave_shr:1 row_mask:0xf bank_mask:0xf bound_ctrl:1
	v_mov_b32_dpp v45, v13 wave_shr:1 row_mask:0xf bank_mask:0xf bound_ctrl:1
	v_mov_b32_dpp v46, v14 wave_shr:1 row_mask:0xf bank_mask:0xf bound_ctrl:1
	v_mov_b32_dpp v68, v12 wave_shl:1 row_mask:0xf bank_mask:0xf bound_ctrl:1
	v_mov_b32_dpp v69, v13 wave_shl:1 row_mask:0xf bank_mask:0xf bound_ctrl:1
	v_mov_b32_dpp v70, v14 wave_shl:1 row_mask:0xf bank_mask:0xf bound_ctrl:1
	s_add_i32 s4, s34, 5
	s_cmpk_lt_u32 s4, 0x201
	s_cselect_b64 s[12:13], s[40:41], 0
	v_cmp_eq_u32_e64 s[14:15], s37, v3
	s_and_b64 s[14:15], s[14:15], s[12:13]
	v_cndmask_b32_e64 v29, 0, 1, s[14:15]
	v_mul_f32_e64 v38, v12, v12
	v_mul_f32_e64 v39, v12, v13
	v_or_b32_dpp v31, v29, v29 wave_shr:1 row_mask:0xf bank_mask:0xf bound_ctrl:1
	v_mul_f32_e64 v50, v12, v14
	v_or_b32_dpp v31, v29, v31 wave_shl:1 row_mask:0xf bank_mask:0xf bound_ctrl:1
	v_mul_f32_e64 v51, v13, v13
	v_mul_f32_e64 v54, v13, v14
	v_or_b32_dpp v85, v31, v31 wave_shr:1 row_mask:0xf bank_mask:0xf bound_ctrl:1
	v_mul_f32_e64 v55, v14, v14
	s_nop 0
	v_or_b32_dpp v85, v31, v85 wave_shl:1 row_mask:0xf bank_mask:0xf bound_ctrl:1
	v_or3_b32 v29, v85, v52, v30
	v_or3_b32 v29, v29, v53, v84
	s_add_i32 s4, s34, 2
	s_cmpk_lt_u32 s4, 0x1ff
	s_cselect_b64 s[12:13], s[42:43], 0
	v_cmp_ne_u32_e64 s[30:31], 0, v29
	s_and_b64 s[30:31], s[30:31], s[12:13]
	v_cndmask_b32_e64 v29, 0, 1.0, s[30:31]
	v_add_f32_e64 v56, v12, v44
	v_add_f32_e64 v57, v13, v45
	v_add_f32_e64 v62, v14, v46
	v_fma_f32 v38, v44, v44, v38
	v_fma_f32 v39, v44, v45, v39
	v_fma_f32 v50, v44, v46, v50
	v_fma_f32 v51, v45, v45, v51
	v_fma_f32 v54, v45, v46, v54
	v_fma_f32 v55, v46, v46, v55
	v_add_f32_dpp v89, v29, v29 wave_shr:1 row_mask:0xf bank_mask:0xf bound_ctrl:1
	v_add_f32_e64 v56, v56, v68
	v_add_f32_e64 v57, v57, v69
	v_add_f32_e64 v62, v62, v70
	v_fma_f32 v63, v68, v68, v38
	v_fma_f32 v66, v68, v69, v39
	v_fma_f32 v67, v68, v70, v50
	v_fma_f32 v86, v69, v69, v51
	v_fma_f32 v87, v69, v70, v54
	v_fma_f32 v88, v70, v70, v55
	v_add_f32_dpp v89, v29, v89 wave_shl:1 row_mask:0xf bank_mask:0xf bound_ctrl:1
	v_pk_add_f32 v[38:39], v[108:109], v[56:57]
	v_pk_add_f32 v[50:51], v[60:61], v[38:39]
	v_pk_add_f32 v[54:55], v[110:111], v[62:63]
	v_pk_add_f32 v[60:61], v[136:137], v[54:55]
	v_pk_add_f32 v[108:109], v[112:113], v[66:67]
	v_pk_add_f32 v[110:111], v[138:139], v[108:109]
	v_pk_add_f32 v[112:113], v[114:115], v[86:87]
	v_pk_add_f32 v[132:133], v[140:141], v[112:113]
	v_pk_add_f32 v[114:115], v[116:117], v[88:89]
	v_pk_add_f32 v[134:135], v[142:143], v[114:115]
	v_mul_f32_e64 v136, v50, v22
	v_mul_f32_e64 v137, v51, v22
	v_mul_f32_e64 v138, v60, v22
	v_fma_f32 v29, v61, v22, v26
	v_mul_f32_e64 v31, v110, v22
	v_mul_f32_e64 v116, v111, v22
	v_fma_f32 v117, v132, v22, v26
	v_mul_f32_e64 v148, v133, v22
	v_fma_f32 v149, v134, v22, v26
	v_fma_f32 v29, -v136, v136, v29
	v_fma_f32 v31, -v136, v137, v31
	v_fma_f32 v116, -v136, v138, v116
	v_fma_f32 v117, -v137, v137, v117
	v_fma_f32 v148, -v137, v138, v148
	v_fma_f32 v149, -v138, v138, v149
	v_mul_f32_e64 v150, v148, v148
	v_mul_f32_e64 v151, v31, v149
	v_mul_f32_e64 v156, v116, v117
	v_mul_f32_e64 v157, v116, v116
	v_mul_f32_e64 v158, v29, v148
	v_mul_f32_e64 v159, v31, v31
	v_fma_f32 v150, v117, v149, -v150
	v_fma_f32 v151, v116, v148, -v151
	v_fma_f32 v156, v31, v148, -v156
	v_fma_f32 v157, v29, v149, -v157
	v_fma_f32 v158, v31, v116, -v158
	v_fma_f32 v159, v29, v117, -v159
	v_mul_f32_e64 v160, v29, v150
	v_fma_f32 v160, v31, v151, v160
	v_fma_f32 v160, v116, v156, v160
	v_rcp_f32_e32 v160, v160
	v_cmp_ne_u32_e64 vcc, s37, v24
	v_mul_f32_e64 v160, v160, v22
	v_cndmask_b32_e64 v160, 0, v160, s[30:31]
	v_cndmask_b32_e64 v29, 0, v18, vcc
	v_cndmask_b32_e64 v145, 0, v22, s[30:31]
	v_mul_f32_e64 v139, v150, v160
	v_mul_f32_e64 v140, v151, v160
	v_mul_f32_e64 v141, v156, v160
	v_mul_f32_e64 v142, v157, v160
	v_mul_f32_e64 v143, v158, v160
	v_mul_f32_e64 v144, v159, v160
	v_add_f32_e64 v146, v135, v29
	v_mov_b32_e32 v147, v24
	ds_write_b128 v23, v[136:139]
	ds_write_b128 v23, v[140:143] offset:1024
	ds_write_b128 v23, v[144:147] offset:2048
	v_mov_b32_dpp v50, v6 wave_shr:1 row_mask:0xf bank_mask:0xf bound_ctrl:1
	v_mov_b32_dpp v51, v7 wave_shr:1 row_mask:0xf bank_mask:0xf bound_ctrl:1
	v_mov_b32_dpp v60, v6 wave_shl:1 row_mask:0xf bank_mask:0xf bound_ctrl:1
	v_mov_b32_dpp v61, v7 wave_shl:1 row_mask:0xf bank_mask:0xf bound_ctrl:1
	v_pk_mul_f32 v[110:111], v[6:7], v[12:13] op_sel_hi:[1,0]
	v_pk_mul_f32 v[116:117], v[6:7], v[12:13] op_sel:[0,1]
	v_pk_mul_f32 v[132:133], v[6:7], v[14:15] op_sel_hi:[1,0]
	v_pk_add_f32 v[134:135], v[6:7], v[50:51]
	v_pk_fma_f32 v[110:111], v[50:51], v[44:45], v[110:111] op_sel_hi:[1,0,1]
	v_pk_fma_f32 v[116:117], v[50:51], v[44:45], v[116:117] op_sel:[0,1,0]
	v_pk_fma_f32 v[132:133], v[50:51], v[46:47], v[132:133] op_sel_hi:[1,0,1]
	v_pk_add_f32 v[134:135], v[134:135], v[60:61]
	v_pk_fma_f32 v[110:111], v[60:61], v[68:69], v[110:111] op_sel_hi:[1,0,1]
	v_pk_fma_f32 v[116:117], v[60:61], v[68:69], v[116:117] op_sel:[0,1,0]
	v_pk_fma_f32 v[132:133], v[60:61], v[70:71], v[132:133] op_sel_hi:[1,0,1]
	s_waitcnt lgkmcnt(0)
	s_barrier
	v_pk_add_f32 v[50:51], v[118:119], v[134:135]
	v_pk_add_f32 v[60:61], v[130:131], v[50:51]
	v_pk_add_f32 v[118:119], v[64:65], v[110:111]
	v_pk_add_f32 v[130:131], v[120:121], v[118:119]
	v_pk_add_f32 v[64:65], v[90:91], v[116:117]
	v_pk_add_f32 v[120:121], v[126:127], v[64:65]
	v_pk_add_f32 v[90:91], v[94:95], v[132:133]
	v_pk_add_f32 v[126:127], v[128:129], v[90:91]
	v_pk_fma_f32 v[130:131], v[136:137], v[60:61], v[130:131] op_sel_hi:[0,1,1] neg_lo:[1,0,0] neg_hi:[1,0,0]
	v_pk_fma_f32 v[120:121], v[136:137], v[60:61], v[120:121] op_sel:[1,0,0] neg_lo:[1,0,0] neg_hi:[1,0,0]
	v_pk_fma_f32 v[126:127], v[138:139], v[60:61], v[126:127] op_sel_hi:[0,1,1] neg_lo:[1,0,0] neg_hi:[1,0,0]
	v_pk_mul_f32 v[94:95], v[138:139], v[130:131] op_sel:[1,0]
	v_pk_mul_f32 v[128:129], v[140:141], v[130:131] op_sel_hi:[0,1]
	v_pk_mul_f32 v[148:149], v[140:141], v[130:131] op_sel:[1,0]
	v_pk_fma_f32 v[94:95], v[140:141], v[120:121], v[94:95] op_sel_hi:[0,1,1]
	v_pk_fma_f32 v[128:129], v[142:143], v[120:121], v[128:129] op_sel_hi:[0,1,1]
	v_pk_fma_f32 v[148:149], v[142:143], v[120:121], v[148:149] op_sel:[1,0,0]
	v_pk_fma_f32 v[94:95], v[140:141], v[126:127], v[94:95] op_sel:[1,0,0]
	v_pk_fma_f32 v[128:129], v[142:143], v[126:127], v[128:129] op_sel:[1,0,0]
	v_pk_fma_f32 v[148:149], v[144:145], v[126:127], v[148:149] op_sel_hi:[0,1,1]
	v_pk_mul_f32 v[150:151], v[136:137], v[94:95] op_sel_hi:[0,1]
	v_pk_fma_f32 v[150:151], v[136:137], v[128:129], v[150:151] op_sel:[1,0,0]
	v_pk_fma_f32 v[150:151], v[138:139], v[148:149], v[150:151] op_sel_hi:[0,1,1]
	v_pk_fma_f32 v[150:151], v[144:145], v[60:61], v[150:151] op_sel:[1,0,0] neg_lo:[0,0,1] neg_hi:[0,0,1]
	v_cmp_eq_u32_e64 s[10:11], 6, v147
	v_cmp_eq_u32_e64 s[14:15], 7, v147
	v_pk_add_f32 v[60:61], v[58:59], v[94:95]
	v_pk_add_f32 v[120:121], v[80:81], v[60:61]
	v_pk_add_f32 v[58:59], v[82:83], v[128:129]
	v_pk_add_f32 v[80:81], v[92:93], v[58:59]
	v_pk_add_f32 v[82:83], v[122:123], v[148:149]
	v_pk_add_f32 v[92:93], v[152:153], v[82:83]
	v_pk_add_f32 v[122:123], v[124:125], v[150:151]
	v_pk_add_f32 v[126:127], v[154:155], v[122:123]
	v_pk_fma_f32 v[124:125], v[72:73], v[120:121], v[126:127] op_sel_hi:[0,1,1]
	v_pk_fma_f32 v[130:131], v[76:77], v[120:121], v[126:127] op_sel_hi:[0,1,1]
	v_pk_fma_f32 v[124:125], v[72:73], v[80:81], v[124:125] op_sel:[1,0,0]
	v_pk_fma_f32 v[130:131], v[76:77], v[80:81], v[130:131] op_sel:[1,0,0]
	v_pk_fma_f32 v[124:125], v[74:75], v[92:93], v[124:125] op_sel_hi:[0,1,1]
	v_pk_fma_f32 v[130:131], v[78:79], v[92:93], v[130:131] op_sel_hi:[0,1,1]
	v_pk_fma_f32 v[126:127], v[104:105], v[120:121], v[126:127] op_sel_hi:[0,1,1]
	v_pk_fma_f32 v[126:127], v[104:105], v[80:81], v[126:127] op_sel:[1,0,0]
	v_pk_fma_f32 v[126:127], v[106:107], v[92:93], v[126:127] op_sel_hi:[0,1,1]
	v_cndmask_b32_e64 v152, 0, v18, s[10:11]
	v_cndmask_b32_e64 v153, 0, v18, s[14:15]
	v_add_f32_dpp v126, v124, v126 wave_shl:1 row_mask:0xf bank_mask:0xf bound_ctrl:1
	v_add_f32_dpp v127, v125, v127 wave_shl:1 row_mask:0xf bank_mask:0xf bound_ctrl:1
	s_add_i32 s4, s34, 2
	s_cmpk_lt_i32 s4, 0x201
	s_cselect_b64 s[12:13], s[0:1], 0
	v_add_f32_dpp v126, v130, v126 wave_shr:1 row_mask:0xf bank_mask:0xf bound_ctrl:1
	v_add_f32_dpp v127, v131, v127 wave_shr:1 row_mask:0xf bank_mask:0xf bound_ctrl:1
	v_pk_fma_f32 v[126:127], v[48:49], v[146:147], v[126:127] op_sel_hi:[1,0,1] neg_lo:[0,0,1] neg_hi:[0,0,1]
	v_pk_add_f32 v[126:127], v[126:127], v[152:153] neg_lo:[0,1] neg_hi:[0,1]
	v_pk_mul_f32 v[154:155], v[126:127], v[126:127]
	v_add_f32_e32 v154, v154, v155
	v_cndmask_b32_e64 v155, 0, v154, s[12:13]
	v_add_f32_e32 v1, v1, v155
	s_add_i32 s5, s34, 7
	s_min_i32 s5, s5, 0x200
	s_mul_i32 s6, s5, 0x804
	s_add_i32 s6, s6, s35
	s_add_i32 s7, s6, 0x505014
	s_add_i32 s8, s6, 0x606018
	s_mul_i32 s9, s5, 0x180c
	s_add_i32 s9, s9, s33
	s_add_i32 s4, s34, 8
	s_min_i32 s4, s4, 0x200
	s_mul_i32 s4, s4, 0x804
	s_add_i32 s4, s4, s38
	buffer_load_dword v24, v28, s[20:23], s4 offen nt
	buffer_load_dwordx3 v[72:74], v27, s[24:27], s9 offen nt
	buffer_load_dword v48, v28, s[16:19], s7 offen nt
	buffer_load_dword v49, v28, s[16:19], s8 offen nt
	s_waitcnt vmcnt(8)
	v_mov_b32_dpp v76, v32 wave_shr:1 row_mask:0xf bank_mask:0xf bound_ctrl:1
	v_mov_b32_dpp v77, v33 wave_shr:1 row_mask:0xf bank_mask:0xf bound_ctrl:1
	v_mov_b32_dpp v78, v34 wave_shr:1 row_mask:0xf bank_mask:0xf bound_ctrl:1
	v_mov_b32_dpp v104, v32 wave_shl:1 row_mask:0xf bank_mask:0xf bound_ctrl:1
	v_mov_b32_dpp v105, v33 wave_shl:1 row_mask:0xf bank_mask:0xf bound_ctrl:1
	v_mov_b32_dpp v106, v34 wave_shl:1 row_mask:0xf bank_mask:0xf bound_ctrl:1
	s_add_i32 s4, s34, 6
	s_cmpk_lt_u32 s4, 0x201
	s_cselect_b64 s[12:13], s[40:41], 0
	v_cmp_eq_u32_e64 s[14:15], s37, v16
	s_and_b64 s[14:15], s[14:15], s[12:13]
	v_cndmask_b32_e64 v29, 0, 1, s[14:15]
	v_mul_f32_e64 v80, v32, v32
	v_mul_f32_e64 v81, v32, v33
	v_or_b32_dpp v31, v29, v29 wave_shr:1 row_mask:0xf bank_mask:0xf bound_ctrl:1
	v_mul_f32_e64 v92, v32, v34
	v_or_b32_dpp v31, v29, v31 wave_shl:1 row_mask:0xf bank_mask:0xf bound_ctrl:1
	v_mul_f32_e64 v93, v33, v33
	v_mul_f32_e64 v120, v33, v34
	v_or_b32_dpp v84, v31, v31 wave_shr:1 row_mask:0xf bank_mask:0xf bound_ctrl:1
	v_mul_f32_e64 v121, v34, v34
	s_nop 0
	v_or_b32_dpp v84, v31, v84 wave_shl:1 row_mask:0xf bank_mask:0xf bound_ctrl:1
	v_or3_b32 v29, v84, v85, v52
	v_or3_b32 v29, v29, v30, v53
	s_add_i32 s4, s34, 3
	s_cmpk_lt_u32 s4, 0x1ff
	s_cselect_b64 s[12:13], s[42:43], 0
	v_cmp_ne_u32_e64 s[30:31], 0, v29
	s_and_b64 s[30:31], s[30:31], s[12:13]
	v_cndmask_b32_e64 v29, 0, 1.0, s[30:31]
	v_add_f32_e64 v124, v32, v76
	v_add_f32_e64 v125, v33, v77
	v_add_f32_e64 v126, v34, v78
	v_fma_f32 v80, v76, v76, v80
	v_fma_f32 v81, v76, v77, v81
	v_fma_f32 v92, v76, v78, v92
	v_fma_f32 v93, v77, v77, v93
	v_fma_f32 v120, v77, v78, v120
	v_fma_f32 v121, v78, v78, v121
	v_add_f32_dpp v139, v29, v29 wave_shr:1 row_mask:0xf bank_mask:0xf bound_ctrl:1
	v_add_f32_e64 v124, v124, v104
	v_add_f32_e64 v125, v125, v105
	v_add_f32_e64 v126, v126, v106
	v_fma_f32 v127, v104, v104, v80
	v_fma_f32 v130, v104, v105, v81
	v_fma_f32 v131, v104, v106, v92
	v_fma_f32 v136, v105, v105, v93
	v_fma_f32 v137, v105, v106, v120
	v_fma_f32 v138, v106, v106, v121
	v_add_f32_dpp v139, v29, v139 wave_shl:1 row_mask:0xf bank_mask:0xf bound_ctrl:1
	v_pk_add_f32 v[80:81], v[38:39], v[124:125]
	v_pk_add_f32 v[38:39], v[54:55], v[126:127]
	v_pk_add_f32 v[54:55], v[108:109], v[130:131]
	v_pk_add_f32 v[92:93], v[112:113], v[136:137]
	v_pk_add_f32 v[108:109], v[114:115], v[138:139]
	v_mul_f32_e64 v112, v80, v22
	v_mul_f32_e64 v113, v81, v22
	v_mul_f32_e64 v114, v38, v22
	v_fma_f32 v29, v39, v22, v26
	v_mul_f32_e64 v31, v54, v22
	v_mul_f32_e64 v120, v55, v22
	v_fma_f32 v121, v92, v22, v26
	v_mul_f32_e64 v152, v93, v22
	v_fma_f32 v153, v108, v22, v26
	v_fma_f32 v29, -v112, v112, v29
	v_fma_f32 v31, -v112, v113, v31
	v_fma_f32 v120, -v112, v114, v120
	v_fma_f32 v121, -v113, v113, v121
	v_fma_f32 v152, -v113, v114, v152
	v_fma_f32 v153, -v114, v114, v153
	v_mul_f32_e64 v154, v152, v152
	v_mul_f32_e64 v155, v31, v153
	v_mul_f32_e64 v156, v120, v121
	v_mul_f32_e64 v157, v120, v120
	v_mul_f32_e64 v158, v29, v152
	v_mul_f32_e64 v159, v31, v31
	v_fma_f32 v154, v121, v153, -v154
	v_fma_f32 v155, v120, v152, -v155
	v_fma_f32 v156, v31, v152, -v156
	v_fma_f32 v157, v29, v153, -v157
	v_fma_f32 v158, v31, v120, -v158
	v_fma_f32 v159, v29, v121, -v159
	v_mul_f32_e64 v160, v29, v154
	v_fma_f32 v160, v31, v155, v160
	v_fma_f32 v160, v120, v156, v160
	v_rcp_f32_e32 v160, v160
	v_cmp_ne_u32_e64 vcc, s37, v17
	v_mul_f32_e64 v160, v160, v22
	v_cndmask_b32_e64 v160, 0, v160, s[30:31]
	v_cndmask_b32_e64 v29, 0, v18, vcc
	v_cndmask_b32_e64 v145, 0, v22, s[30:31]
	v_mul_f32_e64 v115, v154, v160
	v_mul_f32_e64 v140, v155, v160
	v_mul_f32_e64 v141, v156, v160
	v_mul_f32_e64 v142, v157, v160
	v_mul_f32_e64 v143, v158, v160
	v_mul_f32_e64 v144, v159, v160
	v_add_f32_e64 v146, v109, v29
	v_mov_b32_e32 v147, v17
	ds_write_b128 v23, v[112:115] offset:3072
	ds_write_b128 v23, v[140:143] offset:4096
	ds_write_b128 v23, v[144:147] offset:5120
	v_mov_b32_dpp v38, v20 wave_shr:1 row_mask:0xf bank_mask:0xf bound_ctrl:1
	v_mov_b32_dpp v39, v21 wave_shr:1 row_mask:0xf bank_mask:0xf bound_ctrl:1
	v_mov_b32_dpp v54, v20 wave_shl:1 row_mask:0xf bank_mask:0xf bound_ctrl:1
	v_mov_b32_dpp v55, v21 wave_shl:1 row_mask:0xf bank_mask:0xf bound_ctrl:1
	v_pk_mul_f32 v[80:81], v[20:21], v[32:33] op_sel_hi:[1,0]
	v_pk_mul_f32 v[92:93], v[20:21], v[32:33] op_sel:[0,1]
	v_pk_mul_f32 v[108:109], v[20:21], v[34:35] op_sel_hi:[1,0]
	v_pk_add_f32 v[120:121], v[20:21], v[38:39]
	v_pk_fma_f32 v[80:81], v[38:39], v[76:77], v[80:81] op_sel_hi:[1,0,1]
	v_pk_fma_f32 v[92:93], v[38:39], v[76:77], v[92:93] op_sel:[0,1,0]
	v_pk_fma_f32 v[108:109], v[38:39], v[78:79], v[108:109] op_sel_hi:[1,0,1]
	v_pk_add_f32 v[120:121], v[120:121], v[54:55]
	v_pk_fma_f32 v[80:81], v[54:55], v[104:105], v[80:81] op_sel_hi:[1,0,1]
	v_pk_fma_f32 v[92:93], v[54:55], v[104:105], v[92:93] op_sel:[0,1,0]
	v_pk_fma_f32 v[108:109], v[54:55], v[106:107], v[108:109] op_sel_hi:[1,0,1]
	s_waitcnt lgkmcnt(0)
	s_barrier
	v_pk_add_f32 v[38:39], v[50:51], v[120:121]
	v_pk_add_f32 v[50:51], v[118:119], v[80:81]
	v_pk_add_f32 v[54:55], v[64:65], v[92:93]
	v_pk_add_f32 v[64:65], v[90:91], v[108:109]
	v_pk_fma_f32 v[50:51], v[112:113], v[38:39], v[50:51] op_sel_hi:[0,1,1] neg_lo:[1,0,0] neg_hi:[1,0,0]
	v_pk_fma_f32 v[54:55], v[112:113], v[38:39], v[54:55] op_sel:[1,0,0] neg_lo:[1,0,0] neg_hi:[1,0,0]
	v_pk_fma_f32 v[64:65], v[114:115], v[38:39], v[64:65] op_sel_hi:[0,1,1] neg_lo:[1,0,0] neg_hi:[1,0,0]
	v_pk_mul_f32 v[90:91], v[114:115], v[50:51] op_sel:[1,0]
	v_pk_mul_f32 v[118:119], v[140:141], v[50:51] op_sel_hi:[0,1]
	v_pk_mul_f32 v[152:153], v[140:141], v[50:51] op_sel:[1,0]
	v_pk_fma_f32 v[90:91], v[140:141], v[54:55], v[90:91] op_sel_hi:[0,1,1]
	v_pk_fma_f32 v[118:119], v[142:143], v[54:55], v[118:119] op_sel_hi:[0,1,1]
	v_pk_fma_f32 v[152:153], v[142:143], v[54:55], v[152:153] op_sel:[1,0,0]
	v_pk_fma_f32 v[90:91], v[140:141], v[64:65], v[90:91] op_sel:[1,0,0]
	v_pk_fma_f32 v[118:119], v[142:143], v[64:65], v[118:119] op_sel:[1,0,0]
	v_pk_fma_f32 v[152:153], v[144:145], v[64:65], v[152:153] op_sel_hi:[0,1,1]
	v_pk_mul_f32 v[154:155], v[112:113], v[90:91] op_sel_hi:[0,1]
	v_pk_fma_f32 v[154:155], v[112:113], v[118:119], v[154:155] op_sel:[1,0,0]
	v_pk_fma_f32 v[154:155], v[114:115], v[152:153], v[154:155] op_sel_hi:[0,1,1]
	v_pk_fma_f32 v[154:155], v[144:145], v[38:39], v[154:155] op_sel:[1,0,0] neg_lo:[0,0,1] neg_hi:[0,0,1]
	v_cmp_eq_u32_e64 s[10:11], 6, v147
	v_cmp_eq_u32_e64 s[14:15], 7, v147
	v_pk_add_f32 v[38:39], v[60:61], v[90:91]
	v_pk_add_f32 v[50:51], v[58:59], v[118:119]
	v_pk_add_f32 v[54:55], v[82:83], v[152:153]
	v_pk_add_f32 v[58:59], v[122:123], v[154:155]
	v_pk_fma_f32 v[60:61], v[96:97], v[38:39], v[58:59] op_sel_hi:[0,1,1]
	v_pk_fma_f32 v[64:65], v[100:101], v[38:39], v[58:59] op_sel_hi:[0,1,1]
	v_pk_fma_f32 v[60:61], v[96:97], v[50:51], v[60:61] op_sel:[1,0,0]
	v_pk_fma_f32 v[64:65], v[100:101], v[50:51], v[64:65] op_sel:[1,0,0]
	v_pk_fma_f32 v[60:61], v[98:99], v[54:55], v[60:61] op_sel_hi:[0,1,1]
	v_pk_fma_f32 v[64:65], v[102:103], v[54:55], v[64:65] op_sel_hi:[0,1,1]
	v_pk_fma_f32 v[58:59], v[8:9], v[38:39], v[58:59] op_sel_hi:[0,1,1]
	v_pk_fma_f32 v[58:59], v[8:9], v[50:51], v[58:59] op_sel:[1,0,0]
	v_pk_fma_f32 v[58:59], v[10:11], v[54:55], v[58:59] op_sel_hi:[0,1,1]
	v_cndmask_b32_e64 v82, 0, v18, s[10:11]
	v_cndmask_b32_e64 v83, 0, v18, s[14:15]
	v_add_f32_dpp v58, v60, v58 wave_shl:1 row_mask:0xf bank_mask:0xf bound_ctrl:1
	v_add_f32_dpp v59, v61, v59 wave_shl:1 row_mask:0xf bank_mask:0xf bound_ctrl:1
	s_add_i32 s4, s34, 3
	s_cmpk_lt_i32 s4, 0x201
	s_cselect_b64 s[12:13], s[0:1], 0
	v_add_f32_dpp v58, v64, v58 wave_shr:1 row_mask:0xf bank_mask:0xf bound_ctrl:1
	v_add_f32_dpp v59, v65, v59 wave_shr:1 row_mask:0xf bank_mask:0xf bound_ctrl:1
	v_pk_fma_f32 v[58:59], v[4:5], v[146:147], v[58:59] op_sel_hi:[1,0,1] neg_lo:[0,0,1] neg_hi:[0,0,1]
	v_pk_add_f32 v[58:59], v[58:59], v[82:83] neg_lo:[0,1] neg_hi:[0,1]
	v_pk_mul_f32 v[122:123], v[58:59], v[58:59]
	v_add_f32_e32 v122, v122, v123
	v_cndmask_b32_e64 v123, 0, v122, s[12:13]
	v_add_f32_e32 v1, v1, v123
	s_add_i32 s5, s34, 8
	s_min_i32 s5, s5, 0x200
	s_mul_i32 s6, s5, 0x804
	s_add_i32 s6, s6, s35
	s_add_i32 s7, s6, 0x505014
	s_add_i32 s8, s6, 0x606018
	s_mul_i32 s9, s5, 0x180c
	s_add_i32 s9, s9, s33
	s_add_i32 s4, s34, 9
	s_min_i32 s4, s4, 0x200
	s_mul_i32 s4, s4, 0x804
	s_add_i32 s4, s4, s38
	buffer_load_dword v17, v28, s[20:23], s4 offen nt
	buffer_load_dwordx3 v[8:10], v27, s[24:27], s9 offen nt
	buffer_load_dword v4, v28, s[16:19], s7 offen nt
	buffer_load_dword v5, v28, s[16:19], s8 offen nt
	s_waitcnt vmcnt(8)
	v_mov_b32_dpp v96, v40 wave_shr:1 row_mask:0xf bank_mask:0xf bound_ctrl:1
	v_mov_b32_dpp v97, v41 wave_shr:1 row_mask:0xf bank_mask:0xf bound_ctrl:1
	v_mov_b32_dpp v98, v42 wave_shr:1 row_mask:0xf bank_mask:0xf bound_ctrl:1
	v_mov_b32_dpp v100, v40 wave_shl:1 row_mask:0xf bank_mask:0xf bound_ctrl:1
	v_mov_b32_dpp v101, v41 wave_shl:1 row_mask:0xf bank_mask:0xf bound_ctrl:1
	v_mov_b32_dpp v102, v42 wave_shl:1 row_mask:0xf bank_mask:0xf bound_ctrl:1
	s_add_i32 s4, s34, 7
	s_cmpk_lt_u32 s4, 0x201
	s_cselect_b64 s[12:13], s[40:41], 0
	v_cmp_eq_u32_e64 s[14:15], s37, v25
	s_and_b64 s[14:15], s[14:15], s[12:13]
	v_cndmask_b32_e64 v29, 0, 1, s[14:15]
	v_mul_f32_e64 v38, v40, v40
	v_mul_f32_e64 v39, v40, v41
	v_or_b32_dpp v31, v29, v29 wave_shr:1 row_mask:0xf bank_mask:0xf bound_ctrl:1
	v_mul_f32_e64 v50, v40, v42
	v_or_b32_dpp v31, v29, v31 wave_shl:1 row_mask:0xf bank_mask:0xf bound_ctrl:1
	v_mul_f32_e64 v51, v41, v41
	v_mul_f32_e64 v54, v41, v42
	v_or_b32_dpp v53, v31, v31 wave_shr:1 row_mask:0xf bank_mask:0xf bound_ctrl:1
	v_mul_f32_e64 v55, v42, v42
	s_nop 0
	v_or_b32_dpp v53, v31, v53 wave_shl:1 row_mask:0xf bank_mask:0xf bound_ctrl:1
	v_or3_b32 v29, v53, v84, v85
	v_or3_b32 v29, v29, v52, v30
	s_add_i32 s4, s34, 4
	s_cmpk_lt_u32 s4, 0x1ff
	s_cselect_b64 s[12:13], s[42:43], 0
	v_cmp_ne_u32_e64 s[30:31], 0, v29
	s_and_b64 s[30:31], s[30:31], s[12:13]
	v_cndmask_b32_e64 v29, 0, 1.0, s[30:31]
	v_add_f32_e64 v58, v40, v96
	v_add_f32_e64 v59, v41, v97
	v_add_f32_e64 v60, v42, v98
	v_fma_f32 v38, v96, v96, v38
	v_fma_f32 v39, v96, v97, v39
	v_fma_f32 v50, v96, v98, v50
	v_fma_f32 v51, v97, v97, v51
	v_fma_f32 v54, v97, v98, v54
	v_fma_f32 v55, v98, v98, v55
	v_add_f32_dpp v113, v29, v29 wave_shr:1 row_mask:0xf bank_mask:0xf bound_ctrl:1
	v_add_f32_e64 v58, v58, v100
	v_add_f32_e64 v59, v59, v101
	v_add_f32_e64 v60, v60, v102
	v_fma_f32 v61, v100, v100, v38
	v_fma_f32 v64, v100, v101, v39
	v_fma_f32 v65, v100, v102, v50
	v_fma_f32 v82, v101, v101, v51
	v_fma_f32 v83, v101, v102, v54
	v_fma_f32 v112, v102, v102, v55
	v_add_f32_dpp v113, v29, v113 wave_shl:1 row_mask:0xf bank_mask:0xf bound_ctrl:1
	v_pk_add_f32 v[38:39], v[124:125], v[58:59]
	v_pk_add_f32 v[50:51], v[56:57], v[38:39]
	v_pk_add_f32 v[54:55], v[126:127], v[60:61]
	v_pk_add_f32 v[56:57], v[62:63], v[54:55]
	v_pk_add_f32 v[62:63], v[130:131], v[64:65]
	v_pk_add_f32 v[114:115], v[66:67], v[62:63]
	v_pk_add_f32 v[66:67], v[136:137], v[82:83]
	v_pk_add_f32 v[122:123], v[86:87], v[66:67]
	v_pk_add_f32 v[86:87], v[138:139], v[112:113]
	v_pk_add_f32 v[124:125], v[88:89], v[86:87]
	v_mul_f32_e64 v136, v50, v22
	v_mul_f32_e64 v137, v51, v22
	v_mul_f32_e64 v138, v56, v22
	v_fma_f32 v29, v57, v22, v26
	v_mul_f32_e64 v31, v114, v22
	v_mul_f32_e64 v88, v115, v22
	v_fma_f32 v89, v122, v22, v26
	v_mul_f32_e64 v126, v123, v22
	v_fma_f32 v127, v124, v22, v26
	v_fma_f32 v29, -v136, v136, v29
	v_fma_f32 v31, -v136, v137, v31
	v_fma_f32 v88, -v136, v138, v88
	v_fma_f32 v89, -v137, v137, v89
	v_fma_f32 v126, -v137, v138, v126
	v_fma_f32 v127, -v138, v138, v127
	v_mul_f32_e64 v130, v126, v126
	v_mul_f32_e64 v131, v31, v127
	v_mul_f32_e64 v156, v88, v89
	v_mul_f32_e64 v157, v88, v88
	v_mul_f32_e64 v158, v29, v126
	v_mul_f32_e64 v159, v31, v31
	v_fma_f32 v130, v89, v127, -v130
	v_fma_f32 v131, v88, v126, -v131
	v_fma_f32 v156, v31, v126, -v156
	v_fma_f32 v157, v29, v127, -v157
	v_fma_f32 v158, v31, v88, -v158
	v_fma_f32 v159, v29, v89, -v159
	v_mul_f32_e64 v160, v29, v130
	v_fma_f32 v160, v31, v131, v160
	v_fma_f32 v160, v88, v156, v160
	v_rcp_f32_e32 v160, v160
	v_cmp_ne_u32_e64 vcc, s37, v2
	v_mul_f32_e64 v160, v160, v22
	v_cndmask_b32_e64 v160, 0, v160, s[30:31]
	v_cndmask_b32_e64 v29, 0, v18, vcc
	v_cndmask_b32_e64 v145, 0, v22, s[30:31]
	v_mul_f32_e64 v139, v130, v160
	v_mul_f32_e64 v140, v131, v160
	v_mul_f32_e64 v141, v156, v160
	v_mul_f32_e64 v142, v157, v160
	v_mul_f32_e64 v143, v158, v160
	v_mul_f32_e64 v144, v159, v160
	v_add_f32_e64 v146, v125, v29
	v_mov_b32_e32 v147, v2
	ds_write_b128 v23, v[136:139]
	ds_write_b128 v23, v[140:143] offset:1024
	ds_write_b128 v23, v[144:147] offset:2048
	v_mov_b32_dpp v30, v36 wave_shr:1 row_mask:0xf bank_mask:0xf bound_ctrl:1
	v_mov_b32_dpp v31, v37 wave_shr:1 row_mask:0xf bank_mask:0xf bound_ctrl:1
	v_mov_b32_dpp v50, v36 wave_shl:1 row_mask:0xf bank_mask:0xf bound_ctrl:1
	v_mov_b32_dpp v51, v37 wave_shl:1 row_mask:0xf bank_mask:0xf bound_ctrl:1
	v_pk_mul_f32 v[56:57], v[36:37], v[40:41] op_sel_hi:[1,0]
	v_pk_mul_f32 v[88:89], v[36:37], v[40:41] op_sel:[0,1]
	v_pk_mul_f32 v[114:115], v[36:37], v[42:43] op_sel_hi:[1,0]
	v_pk_add_f32 v[122:123], v[36:37], v[30:31]
	v_pk_fma_f32 v[56:57], v[30:31], v[96:97], v[56:57] op_sel_hi:[1,0,1]
	v_pk_fma_f32 v[88:89], v[30:31], v[96:97], v[88:89] op_sel:[0,1,0]
	v_pk_fma_f32 v[114:115], v[30:31], v[98:99], v[114:115] op_sel_hi:[1,0,1]
	v_pk_add_f32 v[122:123], v[122:123], v[50:51]
	v_pk_fma_f32 v[56:57], v[50:51], v[100:101], v[56:57] op_sel_hi:[1,0,1]
	v_pk_fma_f32 v[88:89], v[50:51], v[100:101], v[88:89] op_sel:[0,1,0]
	v_pk_fma_f32 v[114:115], v[50:51], v[102:103], v[114:115] op_sel_hi:[1,0,1]
	s_waitcnt lgkmcnt(0)
	s_barrier
	v_pk_add_f32 v[30:31], v[120:121], v[122:123]
	v_pk_add_f32 v[50:51], v[134:135], v[30:31]
	v_pk_add_f32 v[120:121], v[80:81], v[56:57]
	v_pk_add_f32 v[124:125], v[110:111], v[120:121]
	v_pk_add_f32 v[80:81], v[92:93], v[88:89]
	v_pk_add_f32 v[110:111], v[116:117], v[80:81]
	v_pk_add_f32 v[92:93], v[108:109], v[114:115]
	v_pk_add_f32 v[116:117], v[132:133], v[92:93]
	v_pk_fma_f32 v[124:125], v[136:137], v[50:51], v[124:125] op_sel_hi:[0,1,1] neg_lo:[1,0,0] neg_hi:[1,0,0]
	v_pk_fma_f32 v[110:111], v[136:137], v[50:51], v[110:111] op_sel:[1,0,0] neg_lo:[1,0,0] neg_hi:[1,0,0]
	v_pk_fma_f32 v[116:117], v[138:139], v[50:51], v[116:117] op_sel_hi:[0,1,1] neg_lo:[1,0,0] neg_hi:[1,0,0]
	v_pk_mul_f32 v[108:109], v[138:139], v[124:125] op_sel:[1,0]
	v_pk_mul_f32 v[126:127], v[140:141], v[124:125] op_sel_hi:[0,1]
	v_pk_mul_f32 v[130:131], v[140:141], v[124:125] op_sel:[1,0]
	v_pk_fma_f32 v[108:109], v[140:141], v[110:111], v[108:109] op_sel_hi:[0,1,1]
	v_pk_fma_f32 v[126:127], v[142:143], v[110:111], v[126:127] op_sel_hi:[0,1,1]
	v_pk_fma_f32 v[130:131], v[142:143], v[110:111], v[130:131] op_sel:[1,0,0]
	v_pk_fma_f32 v[108:109], v[140:141], v[116:117], v[108:109] op_sel:[1,0,0]
	v_pk_fma_f32 v[126:127], v[142:143], v[116:117], v[126:127] op_sel:[1,0,0]
	v_pk_fma_f32 v[130:131], v[144:145], v[116:117], v[130:131] op_sel_hi:[0,1,1]
	v_pk_mul_f32 v[132:133], v[136:137], v[108:109] op_sel_hi:[0,1]
	v_pk_fma_f32 v[132:133], v[136:137], v[126:127], v[132:133] op_sel:[1,0,0]
	v_pk_fma_f32 v[132:133], v[138:139], v[130:131], v[132:133] op_sel_hi:[0,1,1]
	v_pk_fma_f32 v[132:133], v[144:145], v[50:51], v[132:133] op_sel:[1,0,0] neg_lo:[0,0,1] neg_hi:[0,0,1]
	v_cmp_eq_u32_e64 s[10:11], 6, v147
	v_cmp_eq_u32_e64 s[14:15], 7, v147
	v_pk_add_f32 v[50:51], v[90:91], v[108:109]
	v_pk_add_f32 v[110:111], v[94:95], v[50:51]
	v_pk_add_f32 v[90:91], v[118:119], v[126:127]
	v_pk_add_f32 v[94:95], v[128:129], v[90:91]
	v_pk_add_f32 v[116:117], v[152:153], v[130:131]
	v_pk_add_f32 v[118:119], v[148:149], v[116:117]
	v_pk_add_f32 v[124:125], v[154:155], v[132:133]
	v_pk_add_f32 v[128:129], v[150:151], v[124:125]
	v_pk_fma_f32 v[134:135], v[44:45], v[110:111], v[128:129] op_sel_hi:[0,1,1]
	v_pk_fma_f32 v[148:149], v[68:69], v[110:111], v[128:129] op_sel_hi:[0,1,1]
	v_pk_fma_f32 v[134:135], v[44:45], v[94:95], v[134:135] op_sel:[1,0,0]
	v_pk_fma_f32 v[148:149], v[68:69], v[94:95], v[148:149] op_sel:[1,0,0]
	v_pk_fma_f32 v[134:135], v[46:47], v[118:119], v[134:135] op_sel_hi:[0,1,1]
	v_pk_fma_f32 v[148:149], v[70:71], v[118:119], v[148:149] op_sel_hi:[0,1,1]
	v_pk_fma_f32 v[128:129], v[12:13], v[110:111], v[128:129] op_sel_hi:[0,1,1]
	v_pk_fma_f32 v[128:129], v[12:13], v[94:95], v[128:129] op_sel:[1,0,0]
	v_pk_fma_f32 v[128:129], v[14:15], v[118:119], v[128:129] op_sel_hi:[0,1,1]
	v_cndmask_b32_e64 v150, 0, v18, s[10:11]
	v_cndmask_b32_e64 v151, 0, v18, s[14:15]
	v_add_f32_dpp v128, v134, v128 wave_shl:1 row_mask:0xf bank_mask:0xf bound_ctrl:1
	v_add_f32_dpp v129, v135, v129 wave_shl:1 row_mask:0xf bank_mask:0xf bound_ctrl:1
	s_add_i32 s4, s34, 4
	s_cmpk_lt_i32 s4, 0x201
	s_cselect_b64 s[12:13], s[0:1], 0
	v_add_f32_dpp v128, v148, v128 wave_shr:1 row_mask:0xf bank_mask:0xf bound_ctrl:1
	v_add_f32_dpp v129, v149, v129 wave_shr:1 row_mask:0xf bank_mask:0xf bound_ctrl:1
	v_pk_fma_f32 v[128:129], v[6:7], v[146:147], v[128:129] op_sel_hi:[1,0,1] neg_lo:[0,0,1] neg_hi:[0,0,1]
	v_pk_add_f32 v[128:129], v[128:129], v[150:151] neg_lo:[0,1] neg_hi:[0,1]
	v_pk_mul_f32 v[152:153], v[128:129], v[128:129]
	v_add_f32_e32 v152, v152, v153
	v_cndmask_b32_e64 v153, 0, v152, s[12:13]
	v_add_f32_e32 v1, v1, v153
	s_add_i32 s5, s34, 9
	s_min_i32 s5, s5, 0x200
	s_mul_i32 s6, s5, 0x804
	s_add_i32 s6, s6, s35
	s_add_i32 s7, s6, 0x505014
	s_add_i32 s8, s6, 0x606018
	s_mul_i32 s9, s5, 0x180c
	s_add_i32 s9, s9, s33
	s_add_i32 s4, s34, 10
	s_min_i32 s4, s4, 0x200
	s_mul_i32 s4, s4, 0x804
	s_add_i32 s4, s4, s38
	buffer_load_dword v2, v28, s[20:23], s4 offen nt
	buffer_load_dwordx3 v[12:14], v27, s[24:27], s9 offen nt
	buffer_load_dword v6, v28, s[16:19], s7 offen nt
	buffer_load_dword v7, v28, s[16:19], s8 offen nt
	s_waitcnt vmcnt(8)
	v_mov_b32_dpp v44, v72 wave_shr:1 row_mask:0xf bank_mask:0xf bound_ctrl:1
	v_mov_b32_dpp v45, v73 wave_shr:1 row_mask:0xf bank_mask:0xf bound_ctrl:1
	v_mov_b32_dpp v46, v74 wave_shr:1 row_mask:0xf bank_mask:0xf bound_ctrl:1
	v_mov_b32_dpp v68, v72 wave_shl:1 row_mask:0xf bank_mask:0xf bound_ctrl:1
	v_mov_b32_dpp v69, v73 wave_shl:1 row_mask:0xf bank_mask:0xf bound_ctrl:1
	v_mov_b32_dpp v70, v74 wave_shl:1 row_mask:0xf bank_mask:0xf bound_ctrl:1
	s_add_i32 s4, s34, 8
	s_cmpk_lt_u32 s4, 0x201
	s_cselect_b64 s[12:13], s[40:41], 0
	v_cmp_eq_u32_e64 s[14:15], s37, v24
	s_and_b64 s[14:15], s[14:15], s[12:13]
	v_cndmask_b32_e64 v29, 0, 1, s[14:15]
	v_mul_f32_e64 v94, v72, v72
	v_mul_f32_e64 v95, v72, v73
	v_or_b32_dpp v128, v29, v29 wave_shr:1 row_mask:0xf bank_mask:0xf bound_ctrl:1
	v_mul_f32_e64 v110, v72, v74
	v_or_b32_dpp v128, v29, v128 wave_shl:1 row_mask:0xf bank_mask:0xf bound_ctrl:1
	v_mul_f32_e64 v111, v73, v73
	v_mul_f32_e64 v118, v73, v74
	v_or_b32_dpp v129, v128, v128 wave_shr:1 row_mask:0xf bank_mask:0xf bound_ctrl:1
	v_mul_f32_e64 v119, v74, v74
	s_nop 0
	v_or_b32_dpp v129, v128, v129 wave_shl:1 row_mask:0xf bank_mask:0xf bound_ctrl:1
	v_or3_b32 v29, v129, v53, v84
	v_or3_b32 v29, v29, v85, v52
	s_add_i32 s4, s34, 5
	s_cmpk_lt_u32 s4, 0x1ff
	s_cselect_b64 s[12:13], s[42:43], 0
	v_cmp_ne_u32_e64 s[30:31], 0, v29
	s_and_b64 s[30:31], s[30:31], s[12:13]
	v_cndmask_b32_e64 v29, 0, 1.0, s[30:31]
	v_add_f32_e64 v134, v72, v44
	v_add_f32_e64 v135, v73, v45
	v_add_f32_e64 v136, v74, v46
	v_fma_f32 v94, v44, v44, v94
	v_fma_f32 v95, v44, v45, v95
	v_fma_f32 v110, v44, v46, v110
	v_fma_f32 v111, v45, v45, v111
	v_fma_f32 v118, v45, v46, v118
	v_fma_f32 v119, v46, v46, v119
	v_add_f32_dpp v143, v29, v29 wave_shr:1 row_mask:0xf bank_mask:0xf bound_ctrl:1
	v_add_f32_e64 v134, v134, v68
	v_add_f32_e64 v135, v135, v69
	v_add_f32_e64 v136, v136, v70
	v_fma_f32 v137, v68, v68, v94
	v_fma_f32 v138, v68, v69, v95
	v_fma_f32 v139, v68, v70, v110
	v_fma_f32 v140, v69, v69, v111
	v_fma_f32 v141, v69, v70, v118
	v_fma_f32 v142, v70, v70, v119
	v_add_f32_dpp v143, v29, v143 wave_shl:1 row_mask:0xf bank_mask:0xf bound_ctrl:1
	v_pk_add_f32 v[94:95], v[38:39], v[134:135]
	v_pk_add_f32 v[38:39], v[54:55], v[136:137]
	v_pk_add_f32 v[54:55], v[62:63], v[138:139]
	v_pk_add_f32 v[62:63], v[66:67], v[140:141]
	v_pk_add_f32 v[66:67], v[86:87], v[142:143]
	v_mul_f32_e64 v144, v94, v22
	v_mul_f32_e64 v145, v95, v22
	v_mul_f32_e64 v146, v38, v22
	v_fma_f32 v29, v39, v22, v26
	v_mul_f32_e64 v128, v54, v22
	v_mul_f32_e64 v86, v55, v22
	v_fma_f32 v87, v62, v22, v26
	v_mul_f32_e64 v110, v63, v22
	v_fma_f32 v111, v66, v22, v26
	v_fma_f32 v29, -v144, v144, v29
	v_fma_f32 v128, -v144, v145, v128
	v_fma_f32 v86, -v144, v146, v86
	v_fma_f32 v87, -v145, v145, v87
	v_fma_f32 v110, -v145, v146, v110
	v_fma_f32 v111, -v146, v146, v111
	v_mul_f32_e64 v118, v110, v110
	v_mul_f32_e64 v119, v128, v111
	v_mul_f32_e64 v156, v86, v87
	v_mul_f32_e64 v157, v86, v86
	v_mul_f32_e64 v158, v29, v110
	v_mul_f32_e64 v159, v128, v128
	v_fma_f32 v118, v87, v111, -v118
	v_fma_f32 v119, v86, v110, -v119
	v_fma_f32 v156, v128, v110, -v156
	v_fma_f32 v157, v29, v111, -v157
	v_fma_f32 v158, v128, v86, -v158
	v_fma_f32 v159, v29, v87, -v159
	v_mul_f32_e64 v160, v29, v118
	v_fma_f32 v160, v128, v119, v160
	v_fma_f32 v160, v86, v156, v160
	v_rcp_f32_e32 v160, v160
	v_cmp_ne_u32_e64 vcc, s37, v3
	v_mul_f32_e64 v160, v160, v22
	v_cndmask_b32_e64 v160, 0, v160, s[30:31]
	v_cndmask_b32_e64 v29, 0, v18, vcc
	v_cndmask_b32_e64 v153, 0, v22, s[30:31]
	v_mul_f32_e64 v147, v118, v160
	v_mul_f32_e64 v148, v119, v160
	v_mul_f32_e64 v149, v156, v160
	v_mul_f32_e64 v150, v157, v160
	v_mul_f32_e64 v151, v158, v160
	v_mul_f32_e64 v152, v159, v160
	v_add_f32_e64 v154, v67, v29
	v_mov_b32_e32 v155, v3
	ds_write_b128 v23, v[144:147] offset:3072
	ds_write_b128 v23, v[148:151] offset:4096
	ds_write_b128 v23, v[152:155] offset:5120
	v_mov_b32_dpp v38, v48 wave_shr:1 row_mask:0xf bank_mask:0xf bound_ctrl:1
	v_mov_b32_dpp v39, v49 wave_shr:1 row_mask:0xf bank_mask:0xf bound_ctrl:1
	v_mov_b32_dpp v54, v48 wave_shl:1 row_mask:0xf bank_mask:0xf bound_ctrl:1
	v_mov_b32_dpp v55, v49 wave_shl:1 row_mask:0xf bank_mask:0xf bound_ctrl:1
	v_pk_mul_f32 v[62:63], v[48:49], v[72:73] op_sel_hi:[1,0]
	v_pk_mul_f32 v[66:67], v[48:49], v[72:73] op_sel:[0,1]
	v_pk_mul_f32 v[86:87], v[48:49], v[74:75] op_sel_hi:[1,0]
	v_pk_add_f32 v[94:95], v[48:49], v[38:39]
	v_pk_fma_f32 v[62:63], v[38:39], v[44:45], v[62:63] op_sel_hi:[1,0,1]
	v_pk_fma_f32 v[66:67], v[38:39], v[44:45], v[66:67] op_sel:[0,1,0]
	v_pk_fma_f32 v[86:87], v[38:39], v[46:47], v[86:87] op_sel_hi:[1,0,1]
	v_pk_add_f32 v[94:95], v[94:95], v[54:55]
	v_pk_fma_f32 v[62:63], v[54:55], v[68:69], v[62:63] op_sel_hi:[1,0,1]
	v_pk_fma_f32 v[66:67], v[54:55], v[68:69], v[66:67] op_sel:[0,1,0]
	v_pk_fma_f32 v[86:87], v[54:55], v[70:71], v[86:87] op_sel_hi:[1,0,1]
	s_waitcnt lgkmcnt(0)
	s_barrier
	v_pk_add_f32 v[38:39], v[30:31], v[94:95]
	v_pk_add_f32 v[30:31], v[120:121], v[62:63]
	v_pk_add_f32 v[54:55], v[80:81], v[66:67]
	v_pk_add_f32 v[80:81], v[92:93], v[86:87]
	v_pk_fma_f32 v[30:31], v[144:145], v[38:39], v[30:31] op_sel_hi:[0,1,1] neg_lo:[1,0,0] neg_hi:[1,0,0]
	v_pk_fma_f32 v[54:55], v[144:145], v[38:39], v[54:55] op_sel:[1,0,0] neg_lo:[1,0,0] neg_hi:[1,0,0]
	v_pk_fma_f32 v[80:81], v[146:147], v[38:39], v[80:81] op_sel_hi:[0,1,1] neg_lo:[1,0,0] neg_hi:[1,0,0]
	v_pk_mul_f32 v[92:93], v[146:147], v[30:31] op_sel:[1,0]
	v_pk_mul_f32 v[110:111], v[148:149], v[30:31] op_sel_hi:[0,1]
	v_pk_mul_f32 v[118:119], v[148:149], v[30:31] op_sel:[1,0]
	v_pk_fma_f32 v[92:93], v[148:149], v[54:55], v[92:93] op_sel_hi:[0,1,1]
	v_pk_fma_f32 v[110:111], v[150:151], v[54:55], v[110:111] op_sel_hi:[0,1,1]
	v_pk_fma_f32 v[118:119], v[150:151], v[54:55], v[118:119] op_sel:[1,0,0]
	v_pk_fma_f32 v[92:93], v[148:149], v[80:81], v[92:93] op_sel:[1,0,0]
	v_pk_fma_f32 v[110:111], v[150:151], v[80:81], v[110:111] op_sel:[1,0,0]
	v_pk_fma_f32 v[118:119], v[152:153], v[80:81], v[118:119] op_sel_hi:[0,1,1]
	v_pk_mul_f32 v[120:121], v[144:145], v[92:93] op_sel_hi:[0,1]
	v_pk_fma_f32 v[120:121], v[144:145], v[110:111], v[120:121] op_sel:[1,0,0]
	v_pk_fma_f32 v[120:121], v[146:147], v[118:119], v[120:121] op_sel_hi:[0,1,1]
	v_pk_fma_f32 v[120:121], v[152:153], v[38:39], v[120:121] op_sel:[1,0,0] neg_lo:[0,0,1] neg_hi:[0,0,1]
	v_cmp_eq_u32_e64 s[10:11], 6, v155
	v_cmp_eq_u32_e64 s[14:15], 7, v155
	v_pk_add_f32 v[30:31], v[50:51], v[92:93]
	v_pk_add_f32 v[38:39], v[90:91], v[110:111]
	v_pk_add_f32 v[50:51], v[116:117], v[118:119]
	v_pk_add_f32 v[54:55], v[124:125], v[120:121]
	v_pk_fma_f32 v[80:81], v[76:77], v[30:31], v[54:55] op_sel_hi:[0,1,1]
	v_pk_fma_f32 v[90:91], v[104:105], v[30:31], v[54:55] op_sel_hi:[0,1,1]
	v_pk_fma_f32 v[80:81], v[76:77], v[38:39], v[80:81] op_sel:[1,0,0]
	v_pk_fma_f32 v[90:91], v[104:105], v[38:39], v[90:91] op_sel:[1,0,0]
	v_pk_fma_f32 v[80:81], v[78:79], v[50:51], v[80:81] op_sel_hi:[0,1,1]
	v_pk_fma_f32 v[90:91], v[106:107], v[50:51], v[90:91] op_sel_hi:[0,1,1]
	v_pk_fma_f32 v[54:55], v[32:33], v[30:31], v[54:55] op_sel_hi:[0,1,1]
	v_pk_fma_f32 v[54:55], v[32:33], v[38:39], v[54:55] op_sel:[1,0,0]
	v_pk_fma_f32 v[54:55], v[34:35], v[50:51], v[54:55] op_sel_hi:[0,1,1]
	v_cndmask_b32_e64 v116, 0, v18, s[10:11]
	v_cndmask_b32_e64 v117, 0, v18, s[14:15]
	v_add_f32_dpp v54, v80, v54 wave_shl:1 row_mask:0xf bank_mask:0xf bound_ctrl:1
	v_add_f32_dpp v55, v81, v55 wave_shl:1 row_mask:0xf bank_mask:0xf bound_ctrl:1
	s_add_i32 s4, s34, 5
	s_cmpk_lt_i32 s4, 0x201
	s_cselect_b64 s[12:13], s[0:1], 0
	v_add_f32_dpp v54, v90, v54 wave_shr:1 row_mask:0xf bank_mask:0xf bound_ctrl:1
	v_add_f32_dpp v55, v91, v55 wave_shr:1 row_mask:0xf bank_mask:0xf bound_ctrl:1
	v_pk_fma_f32 v[54:55], v[20:21], v[154:155], v[54:55] op_sel_hi:[1,0,1] neg_lo:[0,0,1] neg_hi:[0,0,1]
	v_pk_add_f32 v[54:55], v[54:55], v[116:117] neg_lo:[0,1] neg_hi:[0,1]
	v_pk_mul_f32 v[124:125], v[54:55], v[54:55]
	v_add_f32_e32 v124, v124, v125
	v_cndmask_b32_e64 v125, 0, v124, s[12:13]
	v_add_f32_e32 v1, v1, v125
	s_add_i32 s5, s34, 10
	s_min_i32 s5, s5, 0x200
	s_mul_i32 s6, s5, 0x804
	s_add_i32 s6, s6, s35
	s_add_i32 s7, s6, 0x505014
	s_add_i32 s8, s6, 0x606018
	s_mul_i32 s9, s5, 0x180c
	s_add_i32 s9, s9, s33
	s_add_i32 s4, s34, 11
	s_min_i32 s4, s4, 0x200
	s_mul_i32 s4, s4, 0x804
	s_add_i32 s4, s4, s38
	buffer_load_dword v3, v28, s[20:23], s4 offen nt
	buffer_load_dwordx3 v[32:34], v27, s[24:27], s9 offen nt
	buffer_load_dword v20, v28, s[16:19], s7 offen nt
	buffer_load_dword v21, v28, s[16:19], s8 offen nt
	s_waitcnt vmcnt(8)
	v_mov_b32_dpp v76, v8 wave_shr:1 row_mask:0xf bank_mask:0xf bound_ctrl:1
	v_mov_b32_dpp v77, v9 wave_shr:1 row_mask:0xf bank_mask:0xf bound_ctrl:1
	v_mov_b32_dpp v78, v10 wave_shr:1 row_mask:0xf bank_mask:0xf bound_ctrl:1
	v_mov_b32_dpp v104, v8 wave_shl:1 row_mask:0xf bank_mask:0xf bound_ctrl:1
	v_mov_b32_dpp v105, v9 wave_shl:1 row_mask:0xf bank_mask:0xf bound_ctrl:1
	v_mov_b32_dpp v106, v10 wave_shl:1 row_mask:0xf bank_mask:0xf bound_ctrl:1
	s_add_i32 s4, s34, 9
	s_cmpk_lt_u32 s4, 0x201
	s_cselect_b64 s[12:13], s[40:41], 0
	v_cmp_eq_u32_e64 s[14:15], s37, v17
	s_and_b64 s[14:15], s[14:15], s[12:13]
	v_cndmask_b32_e64 v29, 0, 1, s[14:15]
	v_mul_f32_e64 v30, v8, v8
	v_mul_f32_e64 v31, v8, v9
	v_or_b32_dpp v52, v29, v29 wave_shr:1 row_mask:0xf bank_mask:0xf bound_ctrl:1
	v_mul_f32_e64 v38, v8, v10
	v_or_b32_dpp v52, v29, v52 wave_shl:1 row_mask:0xf bank_mask:0xf bound_ctrl:1
	v_mul_f32_e64 v39, v9, v9
	v_mul_f32_e64 v50, v9, v10
	v_or_b32_dpp v128, v52, v52 wave_shr:1 row_mask:0xf bank_mask:0xf bound_ctrl:1
	v_mul_f32_e64 v51, v10, v10
	s_nop 0
	v_or_b32_dpp v128, v52, v128 wave_shl:1 row_mask:0xf bank_mask:0xf bound_ctrl:1
	v_or3_b32 v29, v128, v129, v53
	v_or3_b32 v29, v29, v84, v85
	s_add_i32 s4, s34, 6
	s_cmpk_lt_u32 s4, 0x1ff
	s_cselect_b64 s[12:13], s[42:43], 0
	v_cmp_ne_u32_e64 s[30:31], 0, v29
	s_and_b64 s[30:31], s[30:31], s[12:13]
	v_cndmask_b32_e64 v29, 0, 1.0, s[30:31]
	v_add_f32_e64 v54, v8, v76
	v_add_f32_e64 v55, v9, v77
	v_add_f32_e64 v80, v10, v78
	v_fma_f32 v30, v76, v76, v30
	v_fma_f32 v31, v76, v77, v31
	v_fma_f32 v38, v76, v78, v38
	v_fma_f32 v39, v77, v77, v39
	v_fma_f32 v50, v77, v78, v50
	v_fma_f32 v51, v78, v78, v51
	v_add_f32_dpp v125, v29, v29 wave_shr:1 row_mask:0xf bank_mask:0xf bound_ctrl:1
	v_add_f32_e64 v54, v54, v104
	v_add_f32_e64 v55, v55, v105
	v_add_f32_e64 v80, v80, v106
	v_fma_f32 v81, v104, v104, v30
	v_fma_f32 v90, v104, v105, v31
	v_fma_f32 v91, v104, v106, v38
	v_fma_f32 v116, v105, v105, v39
	v_fma_f32 v117, v105, v106, v50
	v_fma_f32 v124, v106, v106, v51
	v_add_f32_dpp v125, v29, v125 wave_shl:1 row_mask:0xf bank_mask:0xf bound_ctrl:1
	v_pk_add_f32 v[30:31], v[134:135], v[54:55]
	v_pk_add_f32 v[38:39], v[58:59], v[30:31]
	v_pk_add_f32 v[50:51], v[136:137], v[80:81]
	v_pk_add_f32 v[58:59], v[60:61], v[50:51]
	v_pk_add_f32 v[60:61], v[138:139], v[90:91]
	v_pk_add_f32 v[134:135], v[64:65], v[60:61]
	v_pk_add_f32 v[64:65], v[140:141], v[116:117]
	v_pk_add_f32 v[136:137], v[82:83], v[64:65]
	v_pk_add_f32 v[82:83], v[142:143], v[124:125]
	v_pk_add_f32 v[138:139], v[112:113], v[82:83]
	v_mul_f32_e64 v140, v38, v22
	v_mul_f32_e64 v141, v39, v22
	v_mul_f32_e64 v142, v58, v22
	v_fma_f32 v29, v59, v22, v26
	v_mul_f32_e64 v52, v134, v22
	v_mul_f32_e64 v112, v135, v22
	v_fma_f32 v113, v136, v22, v26
	v_mul_f32_e64 v152, v137, v22
	v_fma_f32 v153, v138, v22, v26
	v_fma_f32 v29, -v140, v140, v29
	v_fma_f32 v52, -v140, v141, v52
	v_fma_f32 v112, -v140, v142, v112
	v_fma_f32 v113, -v141, v141, v113
	v_fma_f32 v152, -v141, v142, v152
	v_fma_f32 v153, -v142, v142, v153
	v_mul_f32_e64 v154, v152, v152
	v_mul_f32_e64 v155, v52, v153
	v_mul_f32_e64 v156, v112, v113
	v_mul_f32_e64 v157, v112, v112
	v_mul_f32_e64 v158, v29, v152
	v_mul_f32_e64 v159, v52, v52
	v_fma_f32 v154, v113, v153, -v154
	v_fma_f32 v155, v112, v152, -v155
	v_fma_f32 v156, v52, v152, -v156
	v_fma_f32 v157, v29, v153, -v157
	v_fma_f32 v158, v52, v112, -v158
	v_fma_f32 v159, v29, v113, -v159
	v_mul_f32_e64 v160, v29, v154
	v_fma_f32 v160, v52, v155, v160
	v_fma_f32 v160, v112, v156, v160
	v_rcp_f32_e32 v160, v160
	v_cmp_ne_u32_e64 vcc, s37, v16
	v_mul_f32_e64 v160, v160, v22
	v_cndmask_b32_e64 v160, 0, v160, s[30:31]
	v_cndmask_b32_e64 v29, 0, v18, vcc
	v_cndmask_b32_e64 v149, 0, v22, s[30:31]
	v_mul_f32_e64 v143, v154, v160
	v_mul_f32_e64 v144, v155, v160
	v_mul_f32_e64 v145, v156, v160
	v_mul_f32_e64 v146, v157, v160
	v_mul_f32_e64 v147, v158, v160
	v_mul_f32_e64 v148, v159, v160
	v_add_f32_e64 v150, v139, v29
	v_mov_b32_e32 v151, v16
	ds_write_b128 v23, v[140:143]
	ds_write_b128 v23, v[144:147] offset:1024
	ds_write_b128 v23, v[148:151] offset:2048
	v_mov_b32_dpp v38, v4 wave_shr:1 row_mask:0xf bank_mask:0xf bound_ctrl:1
	v_mov_b32_dpp v39, v5 wave_shr:1 row_mask:0xf bank_mask:0xf bound_ctrl:1
	v_mov_b32_dpp v58, v4 wave_shl:1 row_mask:0xf bank_mask:0xf bound_ctrl:1
	v_mov_b32_dpp v59, v5 wave_shl:1 row_mask:0xf bank_mask:0xf bound_ctrl:1
	v_pk_mul_f32 v[112:113], v[4:5], v[8:9] op_sel_hi:[1,0]
	v_pk_mul_f32 v[134:135], v[4:5], v[8:9] op_sel:[0,1]
	v_pk_mul_f32 v[136:137], v[4:5], v[10:11] op_sel_hi:[1,0]
	v_pk_add_f32 v[138:139], v[4:5], v[38:39]
	v_pk_fma_f32 v[112:113], v[38:39], v[76:77], v[112:113] op_sel_hi:[1,0,1]
	v_pk_fma_f32 v[134:135], v[38:39], v[76:77], v[134:135] op_sel:[0,1,0]
	v_pk_fma_f32 v[136:137], v[38:39], v[78:79], v[136:137] op_sel_hi:[1,0,1]
	v_pk_add_f32 v[138:139], v[138:139], v[58:59]
	v_pk_fma_f32 v[112:113], v[58:59], v[104:105], v[112:113] op_sel_hi:[1,0,1]
	v_pk_fma_f32 v[134:135], v[58:59], v[104:105], v[134:135] op_sel:[0,1,0]
	v_pk_fma_f32 v[136:137], v[58:59], v[106:107], v[136:137] op_sel_hi:[1,0,1]
	s_waitcnt lgkmcnt(0)
	s_barrier
	v_pk_add_f32 v[38:39], v[94:95], v[138:139]
	v_pk_add_f32 v[58:59], v[122:123], v[38:39]
	v_pk_add_f32 v[94:95], v[62:63], v[112:113]
	v_pk_add_f32 v[122:123], v[56:57], v[94:95]
	v_pk_add_f32 v[56:57], v[66:67], v[134:135]
	v_pk_add_f32 v[62:63], v[88:89], v[56:57]
	v_pk_add_f32 v[66:67], v[86:87], v[136:137]
	v_pk_add_f32 v[88:89], v[114:115], v[66:67]
	v_pk_fma_f32 v[122:123], v[140:141], v[58:59], v[122:123] op_sel_hi:[0,1,1] neg_lo:[1,0,0] neg_hi:[1,0,0]
	v_pk_fma_f32 v[62:63], v[140:141], v[58:59], v[62:63] op_sel:[1,0,0] neg_lo:[1,0,0] neg_hi:[1,0,0]
	v_pk_fma_f32 v[88:89], v[142:143], v[58:59], v[88:89] op_sel_hi:[0,1,1] neg_lo:[1,0,0] neg_hi:[1,0,0]
	v_pk_mul_f32 v[86:87], v[142:143], v[122:123] op_sel:[1,0]
	v_pk_mul_f32 v[114:115], v[144:145], v[122:123] op_sel_hi:[0,1]
	v_pk_mul_f32 v[152:153], v[144:145], v[122:123] op_sel:[1,0]
	v_pk_fma_f32 v[86:87], v[144:145], v[62:63], v[86:87] op_sel_hi:[0,1,1]
	v_pk_fma_f32 v[114:115], v[146:147], v[62:63], v[114:115] op_sel_hi:[0,1,1]
	v_pk_fma_f32 v[152:153], v[146:147], v[62:63], v[152:153] op_sel:[1,0,0]
	v_pk_fma_f32 v[86:87], v[144:145], v[88:89], v[86:87] op_sel:[1,0,0]
	v_pk_fma_f32 v[114:115], v[146:147], v[88:89], v[114:115] op_sel:[1,0,0]
	v_pk_fma_f32 v[152:153], v[148:149], v[88:89], v[152:153] op_sel_hi:[0,1,1]
	v_pk_mul_f32 v[154:155], v[140:141], v[86:87] op_sel_hi:[0,1]
	v_pk_fma_f32 v[154:155], v[140:141], v[114:115], v[154:155] op_sel:[1,0,0]
	v_pk_fma_f32 v[154:155], v[142:143], v[152:153], v[154:155] op_sel_hi:[0,1,1]
	v_pk_fma_f32 v[154:155], v[148:149], v[58:59], v[154:155] op_sel:[1,0,0] neg_lo:[0,0,1] neg_hi:[0,0,1]
	v_cmp_eq_u32_e64 s[10:11], 6, v151
	v_cmp_eq_u32_e64 s[14:15], 7, v151
	v_pk_add_f32 v[58:59], v[92:93], v[86:87]
	v_pk_add_f32 v[62:63], v[108:109], v[58:59]
	v_pk_add_f32 v[88:89], v[110:111], v[114:115]
	v_pk_add_f32 v[92:93], v[126:127], v[88:89]
	v_pk_add_f32 v[108:109], v[118:119], v[152:153]
	v_pk_add_f32 v[110:111], v[130:131], v[108:109]
	v_pk_add_f32 v[118:119], v[120:121], v[154:155]
	v_pk_add_f32 v[122:123], v[132:133], v[118:119]
	v_pk_fma_f32 v[120:121], v[96:97], v[62:63], v[122:123] op_sel_hi:[0,1,1]
	v_pk_fma_f32 v[126:127], v[100:101], v[62:63], v[122:123] op_sel_hi:[0,1,1]
	v_pk_fma_f32 v[120:121], v[96:97], v[92:93], v[120:121] op_sel:[1,0,0]
	v_pk_fma_f32 v[126:127], v[100:101], v[92:93], v[126:127] op_sel:[1,0,0]
	v_pk_fma_f32 v[120:121], v[98:99], v[110:111], v[120:121] op_sel_hi:[0,1,1]
	v_pk_fma_f32 v[126:127], v[102:103], v[110:111], v[126:127] op_sel_hi:[0,1,1]
	v_pk_fma_f32 v[122:123], v[40:41], v[62:63], v[122:123] op_sel_hi:[0,1,1]
	v_pk_fma_f32 v[122:123], v[40:41], v[92:93], v[122:123] op_sel:[1,0,0]
	v_pk_fma_f32 v[122:123], v[42:43], v[110:111], v[122:123] op_sel_hi:[0,1,1]
	v_cndmask_b32_e64 v130, 0, v18, s[10:11]
	v_cndmask_b32_e64 v131, 0, v18, s[14:15]
	v_add_f32_dpp v122, v120, v122 wave_shl:1 row_mask:0xf bank_mask:0xf bound_ctrl:1
	v_add_f32_dpp v123, v121, v123 wave_shl:1 row_mask:0xf bank_mask:0xf bound_ctrl:1
	s_add_i32 s4, s34, 6
	s_cmpk_lt_i32 s4, 0x201
	s_cselect_b64 s[12:13], s[0:1], 0
	v_add_f32_dpp v122, v126, v122 wave_shr:1 row_mask:0xf bank_mask:0xf bound_ctrl:1
	v_add_f32_dpp v123, v127, v123 wave_shr:1 row_mask:0xf bank_mask:0xf bound_ctrl:1
	v_pk_fma_f32 v[122:123], v[36:37], v[150:151], v[122:123] op_sel_hi:[1,0,1] neg_lo:[0,0,1] neg_hi:[0,0,1]
	v_pk_add_f32 v[122:123], v[122:123], v[130:131] neg_lo:[0,1] neg_hi:[0,1]
	v_pk_mul_f32 v[132:133], v[122:123], v[122:123]
	v_add_f32_e32 v132, v132, v133
	v_cndmask_b32_e64 v133, 0, v132, s[12:13]
	v_add_f32_e32 v1, v1, v133
	s_add_i32 s5, s34, 11
	s_min_i32 s5, s5, 0x200
	s_mul_i32 s6, s5, 0x804
	s_add_i32 s6, s6, s35
	s_add_i32 s7, s6, 0x505014
	s_add_i32 s8, s6, 0x606018
	s_mul_i32 s9, s5, 0x180c
	s_add_i32 s9, s9, s33
	s_add_i32 s4, s34, 12
	s_min_i32 s4, s4, 0x200
	s_mul_i32 s4, s4, 0x804
	s_add_i32 s4, s4, s38
	buffer_load_dword v16, v28, s[20:23], s4 offen nt
	buffer_load_dwordx3 v[40:42], v27, s[24:27], s9 offen nt
	buffer_load_dword v36, v28, s[16:19], s7 offen nt
	buffer_load_dword v37, v28, s[16:19], s8 offen nt
	s_waitcnt vmcnt(8)
	v_mov_b32_dpp v96, v12 wave_shr:1 row_mask:0xf bank_mask:0xf bound_ctrl:1
	v_mov_b32_dpp v97, v13 wave_shr:1 row_mask:0xf bank_mask:0xf bound_ctrl:1
	v_mov_b32_dpp v98, v14 wave_shr:1 row_mask:0xf bank_mask:0xf bound_ctrl:1
	v_mov_b32_dpp v100, v12 wave_shl:1 row_mask:0xf bank_mask:0xf bound_ctrl:1
	v_mov_b32_dpp v101, v13 wave_shl:1 row_mask:0xf bank_mask:0xf bound_ctrl:1
	v_mov_b32_dpp v102, v14 wave_shl:1 row_mask:0xf bank_mask:0xf bound_ctrl:1
	s_add_i32 s4, s34, 10
	s_cmpk_lt_u32 s4, 0x201
	s_cselect_b64 s[12:13], s[40:41], 0
	v_cmp_eq_u32_e64 s[14:15], s37, v2
	s_and_b64 s[14:15], s[14:15], s[12:13]
	v_cndmask_b32_e64 v29, 0, 1, s[14:15]
	v_mul_f32_e64 v62, v12, v12
	v_mul_f32_e64 v63, v12, v13
	v_or_b32_dpp v52, v29, v29 wave_shr:1 row_mask:0xf bank_mask:0xf bound_ctrl:1
	v_mul_f32_e64 v92, v12, v14
	v_or_b32_dpp v52, v29, v52 wave_shl:1 row_mask:0xf bank_mask:0xf bound_ctrl:1
	v_mul_f32_e64 v93, v13, v13
	v_mul_f32_e64 v110, v13, v14
	v_or_b32_dpp v85, v52, v52 wave_shr:1 row_mask:0xf bank_mask:0xf bound_ctrl:1
	v_mul_f32_e64 v111, v14, v14
	s_nop 0
	v_or_b32_dpp v85, v52, v85 wave_shl:1 row_mask:0xf bank_mask:0xf bound_ctrl:1
	v_or3_b32 v29, v85, v128, v129
	v_or3_b32 v29, v29, v53, v84
	s_add_i32 s4, s34, 7
	s_cmpk_lt_u32 s4, 0x1ff
	s_cselect_b64 s[12:13], s[42:43], 0
	v_cmp_ne_u32_e64 s[30:31], 0, v29
	s_and_b64 s[30:31], s[30:31], s[12:13]
	v_cndmask_b32_e64 v29, 0, 1.0, s[30:31]
	v_add_f32_e64 v120, v12, v96
	v_add_f32_e64 v121, v13, v97
	v_add_f32_e64 v122, v14, v98
	v_fma_f32 v62, v96, v96, v62
	v_fma_f32 v63, v96, v97, v63
	v_fma_f32 v92, v96, v98, v92
	v_fma_f32 v93, v97, v97, v93
	v_fma_f32 v110, v97, v98, v110
	v_fma_f32 v111, v98, v98, v111
	v_add_f32_dpp v133, v29, v29 wave_shr:1 row_mask:0xf bank_mask:0xf bound_ctrl:1
	v_add_f32_e64 v120, v120, v100
	v_add_f32_e64 v121, v121, v101
	v_add_f32_e64 v122, v122, v102
	v_fma_f32 v123, v100, v100, v62
	v_fma_f32 v126, v100, v101, v63
	v_fma_f32 v127, v100, v102, v92
	v_fma_f32 v130, v101, v101, v93
	v_fma_f32 v131, v101, v102, v110
	v_fma_f32 v132, v102, v102, v111
	v_add_f32_dpp v133, v29, v133 wave_shl:1 row_mask:0xf bank_mask:0xf bound_ctrl:1
	v_pk_add_f32 v[62:63], v[30:31], v[120:121]
	v_pk_add_f32 v[30:31], v[50:51], v[122:123]
	v_pk_add_f32 v[50:51], v[60:61], v[126:127]
	v_pk_add_f32 v[60:61], v[64:65], v[130:131]
	v_pk_add_f32 v[64:65], v[82:83], v[132:133]
	v_mul_f32_e64 v140, v62, v22
	v_mul_f32_e64 v141, v63, v22
	v_mul_f32_e64 v142, v30, v22
	v_fma_f32 v29, v31, v22, v26
	v_mul_f32_e64 v52, v50, v22
	v_mul_f32_e64 v82, v51, v22
	v_fma_f32 v83, v60, v22, v26
	v_mul_f32_e64 v92, v61, v22
	v_fma_f32 v93, v64, v22, v26
	v_fma_f32 v29, -v140, v140, v29
	v_fma_f32 v52, -v140, v141, v52
	v_fma_f32 v82, -v140, v142, v82
	v_fma_f32 v83, -v141, v141, v83
	v_fma_f32 v92, -v141, v142, v92
	v_fma_f32 v93, -v142, v142, v93
	v_mul_f32_e64 v110, v92, v92
	v_mul_f32_e64 v111, v52, v93
	v_mul_f32_e64 v156, v82, v83
	v_mul_f32_e64 v157, v82, v82
	v_mul_f32_e64 v158, v29, v92
	v_mul_f32_e64 v159, v52, v52
	v_fma_f32 v110, v83, v93, -v110
	v_fma_f32 v111, v82, v92, -v111
	v_fma_f32 v156, v52, v92, -v156
	v_fma_f32 v157, v29, v93, -v157
	v_fma_f32 v158, v52, v82, -v158
	v_fma_f32 v159, v29, v83, -v159
	v_mul_f32_e64 v160, v29, v110
	v_fma_f32 v160, v52, v111, v160
	v_fma_f32 v160, v82, v156, v160
	v_rcp_f32_e32 v160, v160
	v_cmp_ne_u32_e64 vcc, s37, v25
	v_mul_f32_e64 v160, v160, v22
	v_cndmask_b32_e64 v160, 0, v160, s[30:31]
	v_cndmask_b32_e64 v29, 0, v18, vcc
	v_cndmask_b32_e64 v149, 0, v22, s[30:31]
	v_mul_f32_e64 v143, v110, v160
	v_mul_f32_e64 v144, v111, v160
	v_mul_f32_e64 v145, v156, v160
	v_mul_f32_e64 v146, v157, v160
	v_mul_f32_e64 v147, v158, v160
	v_mul_f32_e64 v148, v159, v160
	v_add_f32_e64 v150, v65, v29
	v_mov_b32_e32 v151, v25
	ds_write_b128 v23, v[140:143] offset:3072
	ds_write_b128 v23, v[144:147] offset:4096
	ds_write_b128 v23, v[148:151] offset:5120
	v_mov_b32_dpp v30, v6 wave_shr:1 row_mask:0xf bank_mask:0xf bound_ctrl:1
	v_mov_b32_dpp v31, v7 wave_shr:1 row_mask:0xf bank_mask:0xf bound_ctrl:1
	v_mov_b32_dpp v50, v6 wave_shl:1 row_mask:0xf bank_mask:0xf bound_ctrl:1
	v_mov_b32_dpp v51, v7 wave_shl:1 row_mask:0xf bank_mask:0xf bound_ctrl:1
	v_pk_mul_f32 v[60:61], v[6:7], v[12:13] op_sel_hi:[1,0]
	v_pk_mul_f32 v[62:63], v[6:7], v[12:13] op_sel:[0,1]
	v_pk_mul_f32 v[64:65], v[6:7], v[14:15] op_sel_hi:[1,0]
	v_pk_add_f32 v[82:83], v[6:7], v[30:31]
	v_pk_fma_f32 v[60:61], v[30:31], v[96:97], v[60:61] op_sel_hi:[1,0,1]
	v_pk_fma_f32 v[62:63], v[30:31], v[96:97], v[62:63] op_sel:[0,1,0]
	v_pk_fma_f32 v[64:65], v[30:31], v[98:99], v[64:65] op_sel_hi:[1,0,1]
	v_pk_add_f32 v[82:83], v[82:83], v[50:51]
	v_pk_fma_f32 v[60:61], v[50:51], v[100:101], v[60:61] op_sel_hi:[1,0,1]
	v_pk_fma_f32 v[62:63], v[50:51], v[100:101], v[62:63] op_sel:[0,1,0]
	v_pk_fma_f32 v[64:65], v[50:51], v[102:103], v[64:65] op_sel_hi:[1,0,1]
	s_waitcnt lgkmcnt(0)
	s_barrier
	v_pk_add_f32 v[30:31], v[38:39], v[82:83]
	v_pk_add_f32 v[38:39], v[94:95], v[60:61]
	v_pk_add_f32 v[50:51], v[56:57], v[62:63]
	v_pk_add_f32 v[56:57], v[66:67], v[64:65]
	v_pk_fma_f32 v[38:39], v[140:141], v[30:31], v[38:39] op_sel_hi:[0,1,1] neg_lo:[1,0,0] neg_hi:[1,0,0]
	v_pk_fma_f32 v[50:51], v[140:141], v[30:31], v[50:51] op_sel:[1,0,0] neg_lo:[1,0,0] neg_hi:[1,0,0]
	v_pk_fma_f32 v[56:57], v[142:143], v[30:31], v[56:57] op_sel_hi:[0,1,1] neg_lo:[1,0,0] neg_hi:[1,0,0]
	v_pk_mul_f32 v[66:67], v[142:143], v[38:39] op_sel:[1,0]
	v_pk_mul_f32 v[92:93], v[144:145], v[38:39] op_sel_hi:[0,1]
	v_pk_mul_f32 v[94:95], v[144:145], v[38:39] op_sel:[1,0]
	v_pk_fma_f32 v[66:67], v[144:145], v[50:51], v[66:67] op_sel_hi:[0,1,1]
	v_pk_fma_f32 v[92:93], v[146:147], v[50:51], v[92:93] op_sel_hi:[0,1,1]
	v_pk_fma_f32 v[94:95], v[146:147], v[50:51], v[94:95] op_sel:[1,0,0]
	v_pk_fma_f32 v[66:67], v[144:145], v[56:57], v[66:67] op_sel:[1,0,0]
	v_pk_fma_f32 v[92:93], v[146:147], v[56:57], v[92:93] op_sel:[1,0,0]
	v_pk_fma_f32 v[94:95], v[148:149], v[56:57], v[94:95] op_sel_hi:[0,1,1]
	v_pk_mul_f32 v[110:111], v[140:141], v[66:67] op_sel_hi:[0,1]
	v_pk_fma_f32 v[110:111], v[140:141], v[92:93], v[110:111] op_sel:[1,0,0]
	v_pk_fma_f32 v[110:111], v[142:143], v[94:95], v[110:111] op_sel_hi:[0,1,1]
	v_pk_fma_f32 v[110:111], v[148:149], v[30:31], v[110:111] op_sel:[1,0,0] neg_lo:[0,0,1] neg_hi:[0,0,1]
	v_cmp_eq_u32_e64 s[10:11], 6, v151
	v_cmp_eq_u32_e64 s[14:15], 7, v151
	v_pk_add_f32 v[30:31], v[58:59], v[66:67]
	v_pk_add_f32 v[38:39], v[88:89], v[92:93]
	v_pk_add_f32 v[50:51], v[108:109], v[94:95]
	v_pk_add_f32 v[56:57], v[118:119], v[110:111]
	v_pk_fma_f32 v[58:59], v[44:45], v[30:31], v[56:57] op_sel_hi:[0,1,1]
	v_pk_fma_f32 v[88:89], v[68:69], v[30:31], v[56:57] op_sel_hi:[0,1,1]
	v_pk_fma_f32 v[58:59], v[44:45], v[38:39], v[58:59] op_sel:[1,0,0]
	v_pk_fma_f32 v[88:89], v[68:69], v[38:39], v[88:89] op_sel:[1,0,0]
	v_pk_fma_f32 v[58:59], v[46:47], v[50:51], v[58:59] op_sel_hi:[0,1,1]
	v_pk_fma_f32 v[88:89], v[70:71], v[50:51], v[88:89] op_sel_hi:[0,1,1]
	v_pk_fma_f32 v[56:57], v[72:73], v[30:31], v[56:57] op_sel_hi:[0,1,1]
	v_pk_fma_f32 v[56:57], v[72:73], v[38:39], v[56:57] op_sel:[1,0,0]
	v_pk_fma_f32 v[56:57], v[74:75], v[50:51], v[56:57] op_sel_hi:[0,1,1]
	v_cndmask_b32_e64 v108, 0, v18, s[10:11]
	v_cndmask_b32_e64 v109, 0, v18, s[14:15]
	v_add_f32_dpp v56, v58, v56 wave_shl:1 row_mask:0xf bank_mask:0xf bound_ctrl:1
	v_add_f32_dpp v57, v59, v57 wave_shl:1 row_mask:0xf bank_mask:0xf bound_ctrl:1
	s_add_i32 s4, s34, 7
	s_cmpk_lt_i32 s4, 0x201
	s_cselect_b64 s[12:13], s[0:1], 0
	v_add_f32_dpp v56, v88, v56 wave_shr:1 row_mask:0xf bank_mask:0xf bound_ctrl:1
	v_add_f32_dpp v57, v89, v57 wave_shr:1 row_mask:0xf bank_mask:0xf bound_ctrl:1
	v_pk_fma_f32 v[56:57], v[48:49], v[150:151], v[56:57] op_sel_hi:[1,0,1] neg_lo:[0,0,1] neg_hi:[0,0,1]
	v_pk_add_f32 v[56:57], v[56:57], v[108:109] neg_lo:[0,1] neg_hi:[0,1]
	v_pk_mul_f32 v[118:119], v[56:57], v[56:57]
	v_add_f32_e32 v118, v118, v119
	v_cndmask_b32_e64 v119, 0, v118, s[12:13]
	v_add_f32_e32 v1, v1, v119
	s_waitcnt vmcnt(4)
	v_mov_b32_dpp v44, v32 wave_shr:1 row_mask:0xf bank_mask:0xf bound_ctrl:1
	v_mov_b32_dpp v45, v33 wave_shr:1 row_mask:0xf bank_mask:0xf bound_ctrl:1
	v_mov_b32_dpp v46, v34 wave_shr:1 row_mask:0xf bank_mask:0xf bound_ctrl:1
	v_mov_b32_dpp v48, v32 wave_shl:1 row_mask:0xf bank_mask:0xf bound_ctrl:1
	v_mov_b32_dpp v49, v33 wave_shl:1 row_mask:0xf bank_mask:0xf bound_ctrl:1
	v_mov_b32_dpp v50, v34 wave_shl:1 row_mask:0xf bank_mask:0xf bound_ctrl:1
	s_add_i32 s4, s34, 11
	s_cmpk_lt_u32 s4, 0x201
	s_cselect_b64 s[12:13], s[40:41], 0
	v_cmp_eq_u32_e64 s[14:15], s37, v3
	s_and_b64 s[14:15], s[14:15], s[12:13]
	v_cndmask_b32_e64 v25, 0, 1, s[14:15]
	v_mul_f32_e64 v30, v32, v32
	v_mul_f32_e64 v31, v32, v33
	v_or_b32_dpp v29, v25, v25 wave_shr:1 row_mask:0xf bank_mask:0xf bound_ctrl:1
	v_mul_f32_e64 v38, v32, v34
	v_or_b32_dpp v29, v25, v29 wave_shl:1 row_mask:0xf bank_mask:0xf bound_ctrl:1
	v_mul_f32_e64 v39, v33, v33
	v_mul_f32_e64 v56, v33, v34
	v_or_b32_dpp v52, v29, v29 wave_shr:1 row_mask:0xf bank_mask:0xf bound_ctrl:1
	v_mul_f32_e64 v57, v34, v34
	s_nop 0
	v_or_b32_dpp v52, v29, v52 wave_shl:1 row_mask:0xf bank_mask:0xf bound_ctrl:1
	v_or3_b32 v25, v52, v85, v128
	v_or3_b32 v25, v25, v129, v53
	s_add_i32 s4, s34, 8
	s_cmpk_lt_u32 s4, 0x1ff
	s_cselect_b64 s[12:13], s[42:43], 0
	v_cmp_ne_u32_e64 s[30:31], 0, v25
	s_and_b64 s[30:31], s[30:31], s[12:13]
	v_cndmask_b32_e64 v25, 0, 1.0, s[30:31]
	v_add_f32_e64 v58, v32, v44
	v_add_f32_e64 v59, v33, v45
	v_add_f32_e64 v68, v34, v46
	v_fma_f32 v30, v44, v44, v30
	v_fma_f32 v31, v44, v45, v31
	v_fma_f32 v38, v44, v46, v38
	v_fma_f32 v39, v45, v45, v39
	v_fma_f32 v56, v45, v46, v56
	v_fma_f32 v57, v46, v46, v57
	v_add_f32_dpp v75, v25, v25 wave_shr:1 row_mask:0xf bank_mask:0xf bound_ctrl:1
	v_add_f32_e64 v58, v58, v48
	v_add_f32_e64 v59, v59, v49
	v_add_f32_e64 v68, v68, v50
	v_fma_f32 v69, v48, v48, v30
	v_fma_f32 v70, v48, v49, v31
	v_fma_f32 v71, v48, v50, v38
	v_fma_f32 v72, v49, v49, v39
	v_fma_f32 v73, v49, v50, v56
	v_fma_f32 v74, v50, v50, v57
	v_add_f32_dpp v75, v25, v75 wave_shl:1 row_mask:0xf bank_mask:0xf bound_ctrl:1
	v_pk_add_f32 v[30:31], v[120:121], v[58:59]
	v_pk_add_f32 v[38:39], v[54:55], v[30:31]
	v_pk_add_f32 v[54:55], v[122:123], v[68:69]
	v_pk_add_f32 v[56:57], v[80:81], v[54:55]
	v_pk_add_f32 v[80:81], v[126:127], v[70:71]
	v_pk_add_f32 v[88:89], v[90:91], v[80:81]
	v_pk_add_f32 v[90:91], v[130:131], v[72:73]
	v_pk_add_f32 v[108:109], v[116:117], v[90:91]
	v_pk_add_f32 v[116:117], v[132:133], v[74:75]
	v_pk_add_f32 v[118:119], v[124:125], v[116:117]
	v_mul_f32_e64 v120, v38, v22
	v_mul_f32_e64 v121, v39, v22
	v_mul_f32_e64 v122, v56, v22
	v_fma_f32 v25, v57, v22, v26
	v_mul_f32_e64 v29, v88, v22
	v_mul_f32_e64 v84, v89, v22
	v_fma_f32 v130, v108, v22, v26
	v_mul_f32_e64 v131, v109, v22
	v_fma_f32 v132, v118, v22, v26
	v_fma_f32 v25, -v120, v120, v25
	v_fma_f32 v29, -v120, v121, v29
	v_fma_f32 v84, -v120, v122, v84
	v_fma_f32 v130, -v121, v121, v130
	v_fma_f32 v131, -v121, v122, v131
	v_fma_f32 v132, -v122, v122, v132
	v_mul_f32_e64 v133, v131, v131
	v_mul_f32_e64 v144, v29, v132
	v_mul_f32_e64 v145, v84, v130
	v_mul_f32_e64 v146, v84, v84
	v_mul_f32_e64 v147, v25, v131
	v_mul_f32_e64 v148, v29, v29
	v_fma_f32 v133, v130, v132, -v133
	v_fma_f32 v144, v84, v131, -v144
	v_fma_f32 v145, v29, v131, -v145
	v_fma_f32 v146, v25, v132, -v146
	v_fma_f32 v147, v29, v84, -v147
	v_fma_f32 v148, v25, v130, -v148
	v_mul_f32_e64 v149, v25, v133
	v_fma_f32 v149, v29, v144, v149
	v_fma_f32 v149, v84, v145, v149
	v_rcp_f32_e32 v149, v149
	v_cmp_ne_u32_e64 vcc, s37, v24
	v_mul_f32_e64 v149, v149, v22
	v_cndmask_b32_e64 v149, 0, v149, s[30:31]
	v_cndmask_b32_e64 v25, 0, v18, vcc
	v_cndmask_b32_e64 v141, 0, v22, s[30:31]
	v_mul_f32_e64 v123, v133, v149
	v_mul_f32_e64 v124, v144, v149
	v_mul_f32_e64 v125, v145, v149
	v_mul_f32_e64 v126, v146, v149
	v_mul_f32_e64 v127, v147, v149
	v_mul_f32_e64 v140, v148, v149
	v_add_f32_e64 v142, v119, v25
	v_mov_b32_e32 v143, v24
	ds_write_b128 v23, v[120:123]
	ds_write_b128 v23, v[124:127] offset:1024
	ds_write_b128 v23, v[140:143] offset:2048
	v_mov_b32_dpp v24, v20 wave_shr:1 row_mask:0xf bank_mask:0xf bound_ctrl:1
	v_mov_b32_dpp v25, v21 wave_shr:1 row_mask:0xf bank_mask:0xf bound_ctrl:1
	v_mov_b32_dpp v38, v20 wave_shl:1 row_mask:0xf bank_mask:0xf bound_ctrl:1
	v_mov_b32_dpp v39, v21 wave_shl:1 row_mask:0xf bank_mask:0xf bound_ctrl:1
	v_pk_mul_f32 v[56:57], v[20:21], v[32:33] op_sel_hi:[1,0]
	v_pk_mul_f32 v[88:89], v[20:21], v[32:33] op_sel:[0,1]
	v_pk_mul_f32 v[108:109], v[20:21], v[34:35] op_sel_hi:[1,0]
	v_pk_add_f32 v[118:119], v[20:21], v[24:25]
	v_pk_fma_f32 v[56:57], v[24:25], v[44:45], v[56:57] op_sel_hi:[1,0,1]
	v_pk_fma_f32 v[88:89], v[24:25], v[44:45], v[88:89] op_sel:[0,1,0]
	v_pk_fma_f32 v[108:109], v[24:25], v[46:47], v[108:109] op_sel_hi:[1,0,1]
	v_pk_add_f32 v[118:119], v[118:119], v[38:39]
	v_pk_fma_f32 v[56:57], v[38:39], v[48:49], v[56:57] op_sel_hi:[1,0,1]
	v_pk_fma_f32 v[88:89], v[38:39], v[48:49], v[88:89] op_sel:[0,1,0]
	v_pk_fma_f32 v[108:109], v[38:39], v[50:51], v[108:109] op_sel_hi:[1,0,1]
	s_waitcnt lgkmcnt(0)
	s_barrier
	v_pk_add_f32 v[24:25], v[82:83], v[118:119]
	v_pk_add_f32 v[38:39], v[138:139], v[24:25]
	v_pk_add_f32 v[82:83], v[60:61], v[56:57]
	v_pk_add_f32 v[130:131], v[112:113], v[82:83]
	v_pk_add_f32 v[60:61], v[62:63], v[88:89]
	v_pk_add_f32 v[112:113], v[134:135], v[60:61]
	v_pk_add_f32 v[62:63], v[64:65], v[108:109]
	v_pk_add_f32 v[132:133], v[136:137], v[62:63]
	v_pk_fma_f32 v[130:131], v[120:121], v[38:39], v[130:131] op_sel_hi:[0,1,1] neg_lo:[1,0,0] neg_hi:[1,0,0]
	v_pk_fma_f32 v[112:113], v[120:121], v[38:39], v[112:113] op_sel:[1,0,0] neg_lo:[1,0,0] neg_hi:[1,0,0]
	v_pk_fma_f32 v[132:133], v[122:123], v[38:39], v[132:133] op_sel_hi:[0,1,1] neg_lo:[1,0,0] neg_hi:[1,0,0]
	v_pk_mul_f32 v[64:65], v[122:123], v[130:131] op_sel:[1,0]
	v_pk_mul_f32 v[134:135], v[124:125], v[130:131] op_sel_hi:[0,1]
	v_pk_mul_f32 v[136:137], v[124:125], v[130:131] op_sel:[1,0]
	v_pk_fma_f32 v[64:65], v[124:125], v[112:113], v[64:65] op_sel_hi:[0,1,1]
	v_pk_fma_f32 v[134:135], v[126:127], v[112:113], v[134:135] op_sel_hi:[0,1,1]
	v_pk_fma_f32 v[136:137], v[126:127], v[112:113], v[136:137] op_sel:[1,0,0]
	v_pk_fma_f32 v[64:65], v[124:125], v[132:133], v[64:65] op_sel:[1,0,0]
	v_pk_fma_f32 v[134:135], v[126:127], v[132:133], v[134:135] op_sel:[1,0,0]
	v_pk_fma_f32 v[136:137], v[140:141], v[132:133], v[136:137] op_sel_hi:[0,1,1]
	v_pk_mul_f32 v[138:139], v[120:121], v[64:65] op_sel_hi:[0,1]
	v_pk_fma_f32 v[138:139], v[120:121], v[134:135], v[138:139] op_sel:[1,0,0]
	v_pk_fma_f32 v[138:139], v[122:123], v[136:137], v[138:139] op_sel_hi:[0,1,1]
	v_pk_fma_f32 v[138:139], v[140:141], v[38:39], v[138:139] op_sel:[1,0,0] neg_lo:[0,0,1] neg_hi:[0,0,1]
	v_cmp_eq_u32_e64 s[10:11], 6, v143
	v_cmp_eq_u32_e64 s[14:15], 7, v143
	v_pk_add_f32 v[38:39], v[66:67], v[64:65]
	v_pk_add_f32 v[112:113], v[86:87], v[38:39]
	v_pk_add_f32 v[66:67], v[92:93], v[134:135]
	v_pk_add_f32 v[86:87], v[114:115], v[66:67]
	v_pk_add_f32 v[92:93], v[94:95], v[136:137]
	v_pk_add_f32 v[114:115], v[152:153], v[92:93]
	v_pk_add_f32 v[94:95], v[110:111], v[138:139]
	v_pk_add_f32 v[130:131], v[154:155], v[94:95]
	v_pk_fma_f32 v[110:111], v[76:77], v[112:113], v[130:131] op_sel_hi:[0,1,1]
	v_pk_fma_f32 v[132:133], v[104:105], v[112:113], v[130:131] op_sel_hi:[0,1,1]
	v_pk_fma_f32 v[110:111], v[76:77], v[86:87], v[110:111] op_sel:[1,0,0]
	v_pk_fma_f32 v[132:133], v[104:105], v[86:87], v[132:133] op_sel:[1,0,0]
	v_pk_fma_f32 v[110:111], v[78:79], v[114:115], v[110:111] op_sel_hi:[0,1,1]
	v_pk_fma_f32 v[132:133], v[106:107], v[114:115], v[132:133] op_sel_hi:[0,1,1]
	v_pk_fma_f32 v[130:131], v[8:9], v[112:113], v[130:131] op_sel_hi:[0,1,1]
	v_pk_fma_f32 v[130:131], v[8:9], v[86:87], v[130:131] op_sel:[1,0,0]
	v_pk_fma_f32 v[130:131], v[10:11], v[114:115], v[130:131] op_sel_hi:[0,1,1]
	v_cndmask_b32_e64 v144, 0, v18, s[10:11]
	v_cndmask_b32_e64 v145, 0, v18, s[14:15]
	v_add_f32_dpp v130, v110, v130 wave_shl:1 row_mask:0xf bank_mask:0xf bound_ctrl:1
	v_add_f32_dpp v131, v111, v131 wave_shl:1 row_mask:0xf bank_mask:0xf bound_ctrl:1
	s_add_i32 s4, s34, 8
	s_cmpk_lt_i32 s4, 0x201
	s_cselect_b64 s[12:13], s[0:1], 0
	v_add_f32_dpp v130, v132, v130 wave_shr:1 row_mask:0xf bank_mask:0xf bound_ctrl:1
	v_add_f32_dpp v131, v133, v131 wave_shr:1 row_mask:0xf bank_mask:0xf bound_ctrl:1
	v_pk_fma_f32 v[130:131], v[4:5], v[142:143], v[130:131] op_sel_hi:[1,0,1] neg_lo:[0,0,1] neg_hi:[0,0,1]
	v_pk_add_f32 v[130:131], v[130:131], v[144:145] neg_lo:[0,1] neg_hi:[0,1]
	v_pk_mul_f32 v[146:147], v[130:131], v[130:131]
	v_add_f32_e32 v146, v146, v147
	v_cndmask_b32_e64 v147, 0, v146, s[12:13]
	v_add_f32_e32 v1, v1, v147
	s_waitcnt vmcnt(0)
	v_mov_b32_dpp v8, v40 wave_shr:1 row_mask:0xf bank_mask:0xf bound_ctrl:1
	v_mov_b32_dpp v9, v41 wave_shr:1 row_mask:0xf bank_mask:0xf bound_ctrl:1
	v_mov_b32_dpp v10, v42 wave_shr:1 row_mask:0xf bank_mask:0xf bound_ctrl:1
	v_mov_b32_dpp v76, v40 wave_shl:1 row_mask:0xf bank_mask:0xf bound_ctrl:1
	v_mov_b32_dpp v77, v41 wave_shl:1 row_mask:0xf bank_mask:0xf bound_ctrl:1
	v_mov_b32_dpp v78, v42 wave_shl:1 row_mask:0xf bank_mask:0xf bound_ctrl:1
	s_add_i32 s4, s34, 12
	s_cmpk_lt_u32 s4, 0x201
	s_cselect_b64 s[12:13], s[40:41], 0
	v_cmp_eq_u32_e64 s[14:15], s37, v16
	s_and_b64 s[14:15], s[14:15], s[12:13]
	v_cndmask_b32_e64 v29, 0, 1, s[14:15]
	v_mul_f32_e64 v4, v40, v40
	v_mul_f32_e64 v5, v40, v41
	v_or_b32_dpp v53, v29, v29 wave_shr:1 row_mask:0xf bank_mask:0xf bound_ctrl:1
	v_mul_f32_e64 v86, v40, v42
	v_or_b32_dpp v53, v29, v53 wave_shl:1 row_mask:0xf bank_mask:0xf bound_ctrl:1
	v_mul_f32_e64 v87, v41, v41
	v_mul_f32_e64 v104, v41, v42
	v_or_b32_dpp v84, v53, v53 wave_shr:1 row_mask:0xf bank_mask:0xf bound_ctrl:1
	v_mul_f32_e64 v105, v42, v42
	s_nop 0
	v_or_b32_dpp v84, v53, v84 wave_shl:1 row_mask:0xf bank_mask:0xf bound_ctrl:1
	v_or3_b32 v29, v84, v52, v85
	v_or3_b32 v29, v29, v128, v129
	s_add_i32 s4, s34, 9
	s_cmpk_lt_u32 s4, 0x1ff
	s_cselect_b64 s[12:13], s[42:43], 0
	v_cmp_ne_u32_e64 s[30:31], 0, v29
	s_and_b64 s[30:31], s[30:31], s[12:13]
	v_cndmask_b32_e64 v29, 0, 1.0, s[30:31]
	v_add_f32_e64 v106, v40, v8
	v_add_f32_e64 v107, v41, v9
	v_add_f32_e64 v110, v42, v10
	v_fma_f32 v4, v8, v8, v4
	v_fma_f32 v5, v8, v9, v5
	v_fma_f32 v86, v8, v10, v86
	v_fma_f32 v87, v9, v9, v87
	v_fma_f32 v104, v9, v10, v104
	v_fma_f32 v105, v10, v10, v105
	v_add_f32_dpp v121, v29, v29 wave_shr:1 row_mask:0xf bank_mask:0xf bound_ctrl:1
	v_add_f32_e64 v106, v106, v76
	v_add_f32_e64 v107, v107, v77
	v_add_f32_e64 v110, v110, v78
	v_fma_f32 v111, v76, v76, v4
	v_fma_f32 v112, v76, v77, v5
	v_fma_f32 v113, v76, v78, v86
	v_fma_f32 v114, v77, v77, v87
	v_fma_f32 v115, v77, v78, v104
	v_fma_f32 v120, v78, v78, v105
	v_add_f32_dpp v121, v29, v121 wave_shl:1 row_mask:0xf bank_mask:0xf bound_ctrl:1
	v_pk_add_f32 v[4:5], v[30:31], v[106:107]
	v_pk_add_f32 v[30:31], v[54:55], v[110:111]
	v_pk_add_f32 v[54:55], v[80:81], v[112:113]
	v_pk_add_f32 v[80:81], v[90:91], v[114:115]
	v_pk_add_f32 v[86:87], v[116:117], v[120:121]
	v_mul_f32_e64 v124, v4, v22
	v_mul_f32_e64 v125, v5, v22
	v_mul_f32_e64 v126, v30, v22
	v_fma_f32 v29, v31, v22, v26
	v_mul_f32_e64 v53, v54, v22
	v_mul_f32_e64 v90, v55, v22
	v_fma_f32 v91, v80, v22, v26
	v_mul_f32_e64 v104, v81, v22
	v_fma_f32 v105, v86, v22, v26
	v_fma_f32 v29, -v124, v124, v29
	v_fma_f32 v53, -v124, v125, v53
	v_fma_f32 v90, -v124, v126, v90
	v_fma_f32 v91, -v125, v125, v91
	v_fma_f32 v104, -v125, v126, v104
	v_fma_f32 v105, -v126, v126, v105
	v_mul_f32_e64 v116, v104, v104
	v_mul_f32_e64 v117, v53, v105
	v_mul_f32_e64 v122, v90, v91
	v_mul_f32_e64 v123, v90, v90
	v_mul_f32_e64 v130, v29, v104
	v_mul_f32_e64 v131, v53, v53
	v_fma_f32 v116, v91, v105, -v116
	v_fma_f32 v117, v90, v104, -v117
	v_fma_f32 v122, v53, v104, -v122
	v_fma_f32 v123, v29, v105, -v123
	v_fma_f32 v130, v53, v90, -v130
	v_fma_f32 v131, v29, v91, -v131
	v_mul_f32_e64 v132, v29, v116
	v_fma_f32 v132, v53, v117, v132
	v_fma_f32 v132, v90, v122, v132
	v_rcp_f32_e32 v132, v132
	v_cmp_ne_u32_e64 vcc, s37, v17
	v_mul_f32_e64 v132, v132, v22
	v_cndmask_b32_e64 v132, 0, v132, s[30:31]
	v_cndmask_b32_e64 v29, 0, v18, vcc
	v_cndmask_b32_e64 v145, 0, v22, s[30:31]
	v_mul_f32_e64 v127, v116, v132
	v_mul_f32_e64 v140, v117, v132
	v_mul_f32_e64 v141, v122, v132
	v_mul_f32_e64 v142, v123, v132
	v_mul_f32_e64 v143, v130, v132
	v_mul_f32_e64 v144, v131, v132
	v_add_f32_e64 v146, v87, v29
	v_mov_b32_e32 v147, v17
	ds_write_b128 v23, v[124:127] offset:3072
	ds_write_b128 v23, v[140:143] offset:4096
	ds_write_b128 v23, v[144:147] offset:5120
	v_mov_b32_dpp v4, v36 wave_shr:1 row_mask:0xf bank_mask:0xf bound_ctrl:1
	v_mov_b32_dpp v5, v37 wave_shr:1 row_mask:0xf bank_mask:0xf bound_ctrl:1
	v_mov_b32_dpp v30, v36 wave_shl:1 row_mask:0xf bank_mask:0xf bound_ctrl:1
	v_mov_b32_dpp v31, v37 wave_shl:1 row_mask:0xf bank_mask:0xf bound_ctrl:1
	v_pk_mul_f32 v[54:55], v[36:37], v[40:41] op_sel_hi:[1,0]
	v_pk_mul_f32 v[80:81], v[36:37], v[40:41] op_sel:[0,1]
	v_pk_mul_f32 v[86:87], v[36:37], v[42:43] op_sel_hi:[1,0]
	v_pk_add_f32 v[90:91], v[36:37], v[4:5]
	v_pk_fma_f32 v[54:55], v[4:5], v[8:9], v[54:55] op_sel_hi:[1,0,1]
	v_pk_fma_f32 v[80:81], v[4:5], v[8:9], v[80:81] op_sel:[0,1,0]
	v_pk_fma_f32 v[86:87], v[4:5], v[10:11], v[86:87] op_sel_hi:[1,0,1]
	v_pk_add_f32 v[90:91], v[90:91], v[30:31]
	v_pk_fma_f32 v[54:55], v[30:31], v[76:77], v[54:55] op_sel_hi:[1,0,1]
	v_pk_fma_f32 v[80:81], v[30:31], v[76:77], v[80:81] op_sel:[0,1,0]
	v_pk_fma_f32 v[86:87], v[30:31], v[78:79], v[86:87] op_sel_hi:[1,0,1]
	s_waitcnt lgkmcnt(0)
	s_barrier
	v_pk_add_f32 v[4:5], v[24:25], v[90:91]
	v_pk_add_f32 v[24:25], v[82:83], v[54:55]
	v_pk_add_f32 v[30:31], v[60:61], v[80:81]
	v_pk_add_f32 v[60:61], v[62:63], v[86:87]
	v_pk_fma_f32 v[24:25], v[124:125], v[4:5], v[24:25] op_sel_hi:[0,1,1] neg_lo:[1,0,0] neg_hi:[1,0,0]
	v_pk_fma_f32 v[30:31], v[124:125], v[4:5], v[30:31] op_sel:[1,0,0] neg_lo:[1,0,0] neg_hi:[1,0,0]
	v_pk_fma_f32 v[60:61], v[126:127], v[4:5], v[60:61] op_sel_hi:[0,1,1] neg_lo:[1,0,0] neg_hi:[1,0,0]
	v_pk_mul_f32 v[62:63], v[126:127], v[24:25] op_sel:[1,0]
	v_pk_mul_f32 v[82:83], v[140:141], v[24:25] op_sel_hi:[0,1]
	v_pk_mul_f32 v[104:105], v[140:141], v[24:25] op_sel:[1,0]
	v_pk_fma_f32 v[62:63], v[140:141], v[30:31], v[62:63] op_sel_hi:[0,1,1]
	v_pk_fma_f32 v[82:83], v[142:143], v[30:31], v[82:83] op_sel_hi:[0,1,1]
	v_pk_fma_f32 v[104:105], v[142:143], v[30:31], v[104:105] op_sel:[1,0,0]
	v_pk_fma_f32 v[62:63], v[140:141], v[60:61], v[62:63] op_sel:[1,0,0]
	v_pk_fma_f32 v[82:83], v[142:143], v[60:61], v[82:83] op_sel:[1,0,0]
	v_pk_fma_f32 v[104:105], v[144:145], v[60:61], v[104:105] op_sel_hi:[0,1,1]
	v_pk_mul_f32 v[116:117], v[124:125], v[62:63] op_sel_hi:[0,1]
	v_pk_fma_f32 v[116:117], v[124:125], v[82:83], v[116:117] op_sel:[1,0,0]
	v_pk_fma_f32 v[116:117], v[126:127], v[104:105], v[116:117] op_sel_hi:[0,1,1]
	v_pk_fma_f32 v[116:117], v[144:145], v[4:5], v[116:117] op_sel:[1,0,0] neg_lo:[0,0,1] neg_hi:[0,0,1]
	v_cmp_eq_u32_e64 s[10:11], 6, v147
	v_cmp_eq_u32_e64 s[14:15], 7, v147
	v_pk_add_f32 v[4:5], v[38:39], v[62:63]
	v_pk_add_f32 v[24:25], v[66:67], v[82:83]
	v_pk_add_f32 v[30:31], v[92:93], v[104:105]
	v_pk_add_f32 v[38:39], v[94:95], v[116:117]
	v_pk_fma_f32 v[60:61], v[96:97], v[4:5], v[38:39] op_sel_hi:[0,1,1]
	v_pk_fma_f32 v[66:67], v[100:101], v[4:5], v[38:39] op_sel_hi:[0,1,1]
	v_pk_fma_f32 v[60:61], v[96:97], v[24:25], v[60:61] op_sel:[1,0,0]
	v_pk_fma_f32 v[66:67], v[100:101], v[24:25], v[66:67] op_sel:[1,0,0]
	v_pk_fma_f32 v[60:61], v[98:99], v[30:31], v[60:61] op_sel_hi:[0,1,1]
	v_pk_fma_f32 v[66:67], v[102:103], v[30:31], v[66:67] op_sel_hi:[0,1,1]
	v_pk_fma_f32 v[38:39], v[12:13], v[4:5], v[38:39] op_sel_hi:[0,1,1]
	v_pk_fma_f32 v[38:39], v[12:13], v[24:25], v[38:39] op_sel:[1,0,0]
	v_pk_fma_f32 v[38:39], v[14:15], v[30:31], v[38:39] op_sel_hi:[0,1,1]
	v_cndmask_b32_e64 v92, 0, v18, s[10:11]
	v_cndmask_b32_e64 v93, 0, v18, s[14:15]
	v_add_f32_dpp v38, v60, v38 wave_shl:1 row_mask:0xf bank_mask:0xf bound_ctrl:1
	v_add_f32_dpp v39, v61, v39 wave_shl:1 row_mask:0xf bank_mask:0xf bound_ctrl:1
	s_add_i32 s4, s34, 9
	s_cmpk_lt_i32 s4, 0x201
	s_cselect_b64 s[12:13], s[0:1], 0
	v_add_f32_dpp v38, v66, v38 wave_shr:1 row_mask:0xf bank_mask:0xf bound_ctrl:1
	v_add_f32_dpp v39, v67, v39 wave_shr:1 row_mask:0xf bank_mask:0xf bound_ctrl:1
	v_pk_fma_f32 v[38:39], v[6:7], v[146:147], v[38:39] op_sel_hi:[1,0,1] neg_lo:[0,0,1] neg_hi:[0,0,1]
	v_pk_add_f32 v[38:39], v[38:39], v[92:93] neg_lo:[0,1] neg_hi:[0,1]
	v_pk_mul_f32 v[94:95], v[38:39], v[38:39]
	v_add_f32_e32 v94, v94, v95
	v_cndmask_b32_e64 v95, 0, v94, s[12:13]
	v_add_f32_e32 v1, v1, v95
	v_mov_b32_e32 v0, v1
	s_branch .LBB0_29
